# speedup vs baseline: 1.0170x; 1.0094x over previous
_Z11prep_kernelPKfS0_S0_S0_PDF16_S1_S0_S1_:
	s_getpc_b64 s[24:25]
	v_lshlrev_b32_e32 v172, 7, v0
	v_min_u32_e32 v172, 0x5800, v172
	global_load_dword v173, v172, s[24:25]
	s_load_dwordx8 s[4:11], s[0:1], 0x0
	s_load_dwordx4 s[12:15], s[0:1], 0x20
	s_mov_b32 s3, 0
	s_lshl_b64 s[2:3], s[2:3], 6
	v_mov_b32_e32 v187, v0
	v_cmp_gt_u32_e32 vcc, 8, v0
	v_lshlrev_b32_e32 v1, 3, v0
	s_and_saveexec_b64 s[16:17], vcc
	s_cbranch_execz .LBB0_2
	s_load_dwordx4 s[20:23], s[0:1], 0x30
	v_or_b32_e32 v10, s2, v1
	v_mov_b32_e32 v11, s3
	s_waitcnt lgkmcnt(0)
	v_lshl_add_u64 v[12:13], v[10:11], 2, s[20:21]
	global_load_dwordx4 v[176:179], v[12:13], off
	global_load_dwordx4 v[180:183], v[12:13], off offset:16
	v_lshl_add_u64 v[184:185], v[10:11], 1, s[22:23]
.LBB0_2:
	s_or_b64 exec, exec, s[16:17]
	v_bfe_u32 v141, v0, 5, 1
	v_lshrrev_b32_e32 v4, 1, v0
	v_lshlrev_b32_e32 v72, 12, v141
	v_mov_b32_e32 v73, 0
	v_and_b32_e32 v142, 0x60, v4
	v_and_b32_e32 v76, 31, v0
	s_waitcnt lgkmcnt(0)
	v_lshl_add_u64 v[2:3], s[10:11], 0, v[72:73]
	v_lshlrev_b32_e32 v72, 2, v142
	v_lshl_add_u64 v[2:3], v[2:3], 0, v[72:73]
	v_lshlrev_b32_e32 v4, 2, v76
	v_mov_b32_e32 v5, v73
	v_lshl_add_u64 v[2:3], v[2:3], 0, v[4:5]
	s_movk_i32 s0, 0x2000
	v_add_co_u32_e32 v4, vcc, s0, v2
	v_and_b32_e32 v1, 0x78, v1
	s_nop 0
	v_addc_co_u32_e32 v5, vcc, 0, v3, vcc
	v_lshrrev_b32_e32 v40, 4, v0
	global_load_dword v140, v[2:3], off
	global_load_dword v136, v[2:3], off offset:512
	global_load_dword v137, v[2:3], off offset:1024
	global_load_dword v138, v[2:3], off offset:1536
	global_load_dword v139, v[2:3], off offset:2048
	global_load_dword v133, v[2:3], off offset:2560
	global_load_dword v134, v[2:3], off offset:3072
	global_load_dword v135, v[2:3], off offset:3584
	global_load_dword v120, v[4:5], off
	global_load_dword v121, v[4:5], off offset:512
	global_load_dword v122, v[4:5], off offset:1024
	global_load_dword v123, v[4:5], off offset:1536
	global_load_dword v124, v[4:5], off offset:2048
	global_load_dword v117, v[4:5], off offset:2560
	global_load_dword v118, v[4:5], off offset:3072
	global_load_dword v119, v[4:5], off offset:3584
	v_lshlrev_b32_e32 v4, 2, v1
	v_mov_b32_e32 v5, v73
	v_or_b32_e32 v74, s2, v40
	v_mov_b32_e32 v75, s3
	s_movk_i32 s0, 0x4000
	v_lshl_add_u64 v[4:5], s[4:5], 0, v[4:5]
	v_lshlrev_b64 v[8:9], 9, v[74:75]
	v_add_co_u32_e32 v6, vcc, s0, v2
	v_lshl_add_u64 v[8:9], v[4:5], 0, v[8:9]
	s_nop 0
	v_addc_co_u32_e32 v7, vcc, 0, v3, vcc
	global_load_dwordx4 v[10:13], v[8:9], off offset:16 nt
	global_load_dwordx4 v[14:17], v[8:9], off nt
	global_load_dword v132, v[6:7], off
	global_load_dword v128, v[6:7], off offset:512
	global_load_dword v129, v[6:7], off offset:1024
	global_load_dword v130, v[6:7], off offset:1536
	global_load_dword v131, v[6:7], off offset:2048
	global_load_dword v125, v[6:7], off offset:2560
	global_load_dword v126, v[6:7], off offset:3072
	global_load_dword v127, v[6:7], off offset:3584
	s_movk_i32 s0, 0x6000
	v_add_co_u32_e32 v6, vcc, s0, v2
	s_mov_b32 s0, 0x8000
	s_nop 0
	v_addc_co_u32_e32 v7, vcc, 0, v3, vcc
	global_load_dword v112, v[6:7], off
	global_load_dword v113, v[6:7], off offset:512
	global_load_dword v114, v[6:7], off offset:1024
	global_load_dword v115, v[6:7], off offset:1536
	global_load_dword v116, v[6:7], off offset:2048
	global_load_dword v109, v[6:7], off offset:2560
	global_load_dword v110, v[6:7], off offset:3072
	global_load_dword v111, v[6:7], off offset:3584
	v_add_co_u32_e32 v6, vcc, s0, v2
	s_mov_b32 s0, 0xa000
	s_nop 0
	v_addc_co_u32_e32 v7, vcc, 0, v3, vcc
	global_load_dword v108, v[6:7], off
	global_load_dword v104, v[6:7], off offset:512
	global_load_dword v105, v[6:7], off offset:1024
	global_load_dword v106, v[6:7], off offset:1536
	global_load_dword v107, v[6:7], off offset:2048
	global_load_dword v101, v[6:7], off offset:2560
	global_load_dword v102, v[6:7], off offset:3072
	global_load_dword v103, v[6:7], off offset:3584
	v_add_co_u32_e32 v6, vcc, s0, v2
	v_mov_b32_e32 v9, v73
	s_nop 0
	v_addc_co_u32_e32 v7, vcc, 0, v3, vcc
	global_load_dword v91, v[6:7], off
	global_load_dword v92, v[6:7], off offset:512
	global_load_dword v93, v[6:7], off offset:1024
	global_load_dword v94, v[6:7], off offset:1536
	global_load_dword v95, v[6:7], off offset:2048
	global_load_dword v88, v[6:7], off offset:2560
	global_load_dword v89, v[6:7], off offset:3072
	global_load_dword v90, v[6:7], off offset:3584
	v_or_b32_e32 v6, 0x100, v0
	v_lshrrev_b32_e32 v8, 4, v6
	v_lshl_add_u64 v[38:39], s[2:3], 0, v[8:9]
	v_lshlrev_b64 v[6:7], 9, v[38:39]
	v_lshl_add_u64 v[6:7], v[4:5], 0, v[6:7]
	global_load_dwordx4 v[18:21], v[6:7], off offset:16 nt
	global_load_dwordx4 v[22:25], v[6:7], off nt
	s_mov_b32 s0, 0xc000
	v_add_co_u32_e32 v6, vcc, s0, v2
	s_mov_b32 s0, 0xe000
	s_nop 0
	v_addc_co_u32_e32 v7, vcc, 0, v3, vcc
	v_add_co_u32_e32 v2, vcc, s0, v2
	global_load_dword v100, v[6:7], off
	global_load_dword v96, v[6:7], off offset:512
	global_load_dword v97, v[6:7], off offset:1024
	global_load_dword v98, v[6:7], off offset:1536
	global_load_dword v99, v[6:7], off offset:2048
	global_load_dword v85, v[6:7], off offset:2560
	global_load_dword v86, v[6:7], off offset:3072
	global_load_dword v87, v[6:7], off offset:3584
	v_addc_co_u32_e32 v3, vcc, 0, v3, vcc
	global_load_dword v80, v[2:3], off
	global_load_dword v81, v[2:3], off offset:512
	global_load_dword v82, v[2:3], off offset:1024
	global_load_dword v83, v[2:3], off offset:1536
	global_load_dword v84, v[2:3], off offset:2048
	global_load_dword v77, v[2:3], off offset:2560
	global_load_dword v78, v[2:3], off offset:3072
	global_load_dword v79, v[2:3], off offset:3584
	v_lshlrev_b32_e32 v2, 1, v1
	v_mov_b32_e32 v3, v73
	v_lshl_add_u64 v[6:7], s[14:15], 0, v[2:3]
	v_lshlrev_b64 v[30:31], 8, v[74:75]
	v_lshl_add_u64 v[30:31], v[6:7], 0, v[30:31]
	v_mov_b32_e32 v45, v73
	s_mov_b32 s0, 0x41800000
	s_mov_b32 s1, 0x3b800000
	s_movk_i32 s4, 0x110
	v_or_b32_e32 v3, 0x4400, v2
	s_waitcnt vmcnt(51)
	v_cvt_pk_f16_f32 v28, v10, v11
	s_waitcnt vmcnt(50)
	v_cvt_pk_f16_f32 v26, v14, v15
	v_cvt_pk_f16_f32 v27, v16, v17
	v_cvt_pk_f16_f32 v29, v12, v13
	global_store_dwordx4 v[30:31], v[26:29], off
	v_mul_f32_e32 v1, 0x41800000, v14
	v_mul_f32_e32 v9, 0x41800000, v15
	v_or_b32_e32 v26, 0x200, v0
	v_lshrrev_b32_e32 v44, 4, v26
	v_lshl_add_u64 v[46:47], s[2:3], 0, v[44:45]
	v_lshlrev_b64 v[26:27], 9, v[46:47]
	v_lshl_add_u64 v[34:35], v[4:5], 0, v[26:27]
	global_load_dwordx4 v[26:29], v[34:35], off offset:16 nt
	global_load_dwordx4 v[30:33], v[34:35], off nt
	v_mul_f32_e32 v35, 0x41800000, v16
	v_mul_f32_e32 v36, 0x41800000, v17
	v_cvt_pk_f16_f32 v34, v1, v9
	v_mul_f32_e32 v37, 0x41800000, v10
	v_fma_mix_f32 v1, v14, s0, -v34 op_sel_hi:[0,0,1]
	v_mul_f32_e32 v41, 0x41800000, v11
	v_cvt_pk_f16_f32 v35, v35, v36
	v_cvt_pk_f16_f32 v36, v37, v41
	v_fma_mix_f32 v9, v15, s0, -v34 op_sel:[0,0,1] op_sel_hi:[0,0,1]
	v_fma_mix_f32 v14, v16, s0, -v35 op_sel_hi:[0,0,1]
	v_fma_mix_f32 v16, v10, s0, -v36 op_sel_hi:[0,0,1]
	v_cvt_pk_f16_f32 v10, v1, v9
	v_mad_u32_u24 v1, v40, s4, v2
	v_mul_f32_e32 v42, 0x41800000, v12
	v_mul_f32_e32 v43, 0x41800000, v13
	v_cvt_pk_f16_f32 v37, v42, v43
	ds_write_b128 v1, v[34:37]
	v_fma_mix_f32 v13, v13, s0, -v37 op_sel:[0,0,1] op_sel_hi:[0,0,1]
	v_mad_u32_u24 v1, v40, s4, v3
	v_or_b32_e32 v0, 0x300, v0
	v_fma_mix_f32 v15, v17, s0, -v35 op_sel:[0,0,1] op_sel_hi:[0,0,1]
	v_fma_mix_f32 v17, v11, s0, -v36 op_sel:[0,0,1] op_sel_hi:[0,0,1]
	v_fma_mix_f32 v41, v12, s0, -v37 op_sel_hi:[0,0,1]
	v_cvt_pk_f16_f32 v11, v14, v15
	v_cvt_pk_f16_f32 v12, v16, v17
	v_cvt_pk_f16_f32 v13, v41, v13
	ds_write_b128 v1, v[10:13]
	v_lshrrev_b32_e32 v0, 4, v0
	v_mov_b32_e32 v1, v73
	v_lshl_add_u64 v[48:49], s[2:3], 0, v[0:1]
	v_lshlrev_b64 v[10:11], 9, v[48:49]
	v_lshl_add_u64 v[4:5], v[4:5], 0, v[10:11]
	global_load_dwordx4 v[10:13], v[4:5], off offset:16 nt
	global_load_dwordx4 v[14:17], v[4:5], off nt
	v_lshlrev_b64 v[4:5], 8, v[38:39]
	s_waitcnt vmcnt(21)
	v_cvt_pk_f16_f32 v34, v22, v23
	v_lshl_add_u64 v[4:5], v[6:7], 0, v[4:5]
	v_mul_f32_e32 v1, 0x41800000, v22
	v_cvt_pk_f16_f32 v35, v24, v25
	v_cvt_pk_f16_f32 v36, v18, v19
	v_cvt_pk_f16_f32 v37, v20, v21
	global_store_dwordx4 v[4:5], v[34:37], off
	v_mul_f32_e32 v4, 0x41800000, v23
	v_mul_f32_e32 v5, 0x41800000, v24
	v_cvt_pk_f16_f32 v34, v1, v4
	v_mul_f32_e32 v9, 0x41800000, v25
	v_fma_mix_f32 v1, v22, s0, -v34 op_sel_hi:[0,0,1]
	v_fma_mix_f32 v4, v23, s0, -v34 op_sel:[0,0,1] op_sel_hi:[0,0,1]
	v_cvt_pk_f16_f32 v22, v1, v4
	v_or_b32_e32 v1, v142, v76
	v_mul_f32_e32 v36, 0x41800000, v18
	v_cvt_pk_f16_f32 v35, v5, v9
	v_lshlrev_b32_e32 v4, 9, v1
	v_mov_b32_e32 v5, v73
	v_mul_f32_e32 v37, 0x41800000, v19
	v_mul_f32_e32 v38, 0x41800000, v20
	v_mul_f32_e32 v39, 0x41800000, v21
	v_cvt_pk_f16_f32 v36, v36, v37
	v_fma_mix_f32 v9, v24, s0, -v35 op_sel_hi:[0,0,1]
	v_fma_mix_f32 v23, v25, s0, -v35 op_sel:[0,0,1] op_sel_hi:[0,0,1]
	v_fma_mix_f32 v24, v18, s0, -v36 op_sel_hi:[0,0,1]
	v_fma_mix_f32 v25, v19, s0, -v36 op_sel:[0,0,1] op_sel_hi:[0,0,1]
	v_lshl_add_u64 v[4:5], s[6:7], 0, v[4:5]
	v_lshlrev_b32_e32 v18, 5, v141
	v_mov_b32_e32 v19, v73
	v_cvt_pk_f16_f32 v37, v38, v39
	v_mad_u32_u24 v1, v8, s4, v2
	v_fma_mix_f32 v38, v20, s0, -v37 op_sel_hi:[0,0,1]
	v_fma_mix_f32 v39, v21, s0, -v37 op_sel:[0,0,1] op_sel_hi:[0,0,1]
	v_lshl_add_u64 v[20:21], v[4:5], 0, v[18:19]
	global_load_dwordx4 v[64:67], v[20:21], off
	global_load_dwordx4 v[40:43], v[20:21], off offset:16
	v_lshlrev_b64 v[4:5], 8, v[46:47]
	v_cvt_pk_f16_f32 v23, v9, v23
	v_cvt_pk_f16_f32 v24, v24, v25
	v_cvt_pk_f16_f32 v25, v38, v39
	ds_write_b128 v1, v[34:37]
	v_mad_u32_u24 v1, v8, s4, v3
	v_lshl_add_u64 v[4:5], v[6:7], 0, v[4:5]
	ds_write_b128 v1, v[22:25]
	s_waitcnt vmcnt(5)
	v_cvt_pk_f16_f32 v22, v30, v31
	v_cvt_pk_f16_f32 v23, v32, v33
	v_cvt_pk_f16_f32 v24, v26, v27
	v_cvt_pk_f16_f32 v25, v28, v29
	global_store_dwordx4 v[4:5], v[22:25], off
	v_mul_f32_e32 v4, 0x41800000, v31
	v_mul_f32_e32 v5, 0x41800000, v32
	v_mul_f32_e32 v1, 0x41800000, v30
	v_mul_f32_e32 v8, 0x41800000, v33
	v_mul_f32_e32 v9, 0x41800000, v26
	v_mul_f32_e32 v18, 0x41800000, v27
	v_cvt_pk_f16_f32 v22, v1, v4
	v_cvt_pk_f16_f32 v23, v5, v8
	global_load_dwordx4 v[52:55], v[20:21], off offset:64
	v_fma_mix_f32 v4, v31, s0, -v22 op_sel:[0,0,1] op_sel_hi:[0,0,1]
	v_fma_mix_f32 v5, v32, s0, -v23 op_sel_hi:[0,0,1]
	v_cvt_pk_f16_f32 v24, v9, v18
	v_fma_mix_f32 v1, v30, s0, -v22 op_sel_hi:[0,0,1]
	v_fma_mix_f32 v8, v33, s0, -v23 op_sel:[0,0,1] op_sel_hi:[0,0,1]
	v_fma_mix_f32 v9, v26, s0, -v24 op_sel_hi:[0,0,1]
	v_fma_mix_f32 v18, v27, s0, -v24 op_sel:[0,0,1] op_sel_hi:[0,0,1]
	v_cvt_pk_f16_f32 v26, v1, v4
	v_cvt_pk_f16_f32 v27, v5, v8
	v_lshlrev_b64 v[4:5], 8, v[48:49]
	global_load_dwordx4 v[48:51], v[20:21], off offset:80
	v_mul_f32_e32 v25, 0x41800000, v29
	v_mad_u32_u24 v1, v44, s4, v2
	v_mul_f32_e32 v19, 0x41800000, v28
	v_cvt_pk_f16_f32 v25, v19, v25
	ds_write_b128 v1, v[22:25]
	v_fma_mix_f32 v29, v29, s0, -v25 op_sel:[0,0,1] op_sel_hi:[0,0,1]
	v_mad_u32_u24 v1, v44, s4, v3
	v_lshl_add_u64 v[4:5], v[6:7], 0, v[4:5]
	v_fma_mix_f32 v19, v28, s0, -v25 op_sel_hi:[0,0,1]
	v_cvt_pk_f16_f32 v28, v9, v18
	v_cvt_pk_f16_f32 v29, v19, v29
	ds_write_b128 v1, v[26:29]
	s_waitcnt vmcnt(6)
	v_cvt_pk_f16_f32 v22, v14, v15
	v_cvt_pk_f16_f32 v23, v16, v17
	v_cvt_pk_f16_f32 v24, v10, v11
	v_cvt_pk_f16_f32 v25, v12, v13
	global_store_dwordx4 v[4:5], v[22:25], off
	v_mul_f32_e32 v1, 0x41800000, v14
	v_mul_f32_e32 v4, 0x41800000, v15
	v_mul_f32_e32 v5, 0x41800000, v16
	v_mul_f32_e32 v6, 0x41800000, v17
	v_mul_f32_e32 v8, 0x41800000, v11
	v_mul_f32_e32 v7, 0x41800000, v10
	v_mul_f32_e32 v9, 0x41800000, v12
	v_cvt_pk_f16_f32 v4, v1, v4
	v_cvt_pk_f16_f32 v5, v5, v6
	v_cvt_pk_f16_f32 v6, v7, v8
	v_mul_f32_e32 v18, 0x41800000, v13
	v_fma_mix_f32 v1, v14, s0, -v4 op_sel_hi:[0,0,1]
	v_fma_mix_f32 v8, v15, s0, -v4 op_sel:[0,0,1] op_sel_hi:[0,0,1]
	v_cvt_pk_f16_f32 v7, v9, v18
	v_fma_mix_f32 v9, v16, s0, -v5 op_sel_hi:[0,0,1]
	v_fma_mix_f32 v10, v10, s0, -v6 op_sel_hi:[0,0,1]
	v_fma_mix_f32 v11, v11, s0, -v6 op_sel:[0,0,1] op_sel_hi:[0,0,1]
	v_cvt_pk_f16_f32 v8, v1, v8
	v_mad_u32_u24 v1, v0, s4, v2
	v_mad_u32_u24 v0, v0, s4, v3
	v_fma_mix_f32 v14, v17, s0, -v5 op_sel:[0,0,1] op_sel_hi:[0,0,1]
	v_fma_mix_f32 v12, v12, s0, -v7 op_sel_hi:[0,0,1]
	v_fma_mix_f32 v13, v13, s0, -v7 op_sel:[0,0,1] op_sel_hi:[0,0,1]
	v_cvt_pk_f16_f32 v9, v9, v14
	v_cvt_pk_f16_f32 v10, v10, v11
	v_cvt_pk_f16_f32 v11, v12, v13
	ds_write_b128 v1, v[4:7]
	ds_write_b128 v0, v[8:11]
	s_waitcnt vmcnt(5)
	v_mul_f32_e32 v0, 0x43800000, v64
	v_mul_f32_e32 v1, 0x43800000, v65
	v_mul_f32_e32 v2, 0x43800000, v66
	v_mul_f32_e32 v3, 0x43800000, v67
	s_waitcnt vmcnt(4)
	v_mul_f32_e32 v4, 0x43800000, v40
	v_mul_f32_e32 v5, 0x43800000, v41
	v_mul_f32_e32 v6, 0x43800000, v42
	v_mul_f32_e32 v7, 0x43800000, v43
	v_cvt_pk_f16_f32 v60, v0, v1
	v_cvt_pk_f16_f32 v61, v2, v3
	v_cvt_pk_f16_f32 v62, v4, v5
	v_cvt_pk_f16_f32 v63, v6, v7
	v_cmp_gt_u32_e32 vcc, 8, v187
	s_nop 1
	s_and_saveexec_b64 s[16:17], vcc
	s_cbranch_execz .Lmy_wg_skip
	v_cvt_pk_f16_f32 v176, v176, v177
	v_cvt_pk_f16_f32 v177, v178, v179
	v_cvt_pk_f16_f32 v178, v180, v181
	v_cvt_pk_f16_f32 v179, v182, v183
	global_store_dwordx4 v[184:185], v[176:179], off
.Lmy_wg_skip:
	s_or_b64 exec, exec, s[16:17]
	global_load_dwordx4 v[44:47], v[20:21], off offset:144
	global_load_dwordx4 v[56:59], v[20:21], off offset:128
	global_load_dwordx4 v[0:3], v[20:21], off offset:208
	global_load_dwordx4 v[8:11], v[20:21], off offset:192
	global_load_dwordx4 v[4:7], v[20:21], off offset:272
	global_load_dwordx4 v[12:15], v[20:21], off offset:256
	v_lshl_add_u64 v[16:17], s[8:9], 0, v[72:73]
	v_lshlrev_b32_e32 v72, 4, v141
	v_lshl_add_u64 v[16:17], v[16:17], 0, v[72:73]
	v_mad_u32_u24 v74, v76, s4, v72
	global_load_dwordx4 v[156:159], v[16:17], off
	global_load_dwordx4 v[152:155], v[16:17], off offset:32
	global_load_dwordx4 v[148:151], v[16:17], off offset:64
	global_load_dwordx4 v[144:147], v[16:17], off offset:96
	global_load_dwordx4 v[32:35], v[20:21], off offset:336
	global_load_dwordx4 v[36:39], v[20:21], off offset:320
	global_load_dwordx4 v[24:27], v[20:21], off offset:400
	global_load_dwordx4 v[28:31], v[20:21], off offset:384
	s_nop 0
	global_load_dwordx4 v[16:19], v[20:21], off offset:464
	s_nop 0
	global_load_dwordx4 v[20:23], v[20:21], off offset:448
	s_waitcnt lgkmcnt(0)
	s_barrier
	ds_read_b128 v[68:71], v74
	s_mov_b32 s3, 0x43800000
	v_fma_mix_f32 v143, v64, s3, -v60 op_sel_hi:[0,0,1]
	v_fma_mix_f32 v160, v65, s3, -v60 op_sel:[0,0,1] op_sel_hi:[0,0,1]
	v_fma_mix_f32 v161, v66, s3, -v61 op_sel_hi:[0,0,1]
	v_fma_mix_f32 v162, v67, s3, -v61 op_sel:[0,0,1] op_sel_hi:[0,0,1]
	ds_read_b128 v[64:67], v74 offset:32
	s_waitcnt lgkmcnt(1)
	v_mfma_f32_32x32x16_f16 a[16:31], v[60:63], v[68:71], 0
	v_fma_mix_f32 v163, v40, s3, -v62 op_sel_hi:[0,0,1]
	v_fma_mix_f32 v43, v43, s3, -v63 op_sel:[0,0,1] op_sel_hi:[0,0,1]
	v_fma_mix_f32 v164, v41, s3, -v62 op_sel:[0,0,1] op_sel_hi:[0,0,1]
	v_fma_mix_f32 v165, v42, s3, -v63 op_sel_hi:[0,0,1]
	v_cvt_pk_f16_f32 v40, v143, v160
	v_cvt_pk_f16_f32 v41, v161, v162
	v_cvt_pk_f16_f32 v42, v163, v164
	v_cvt_pk_f16_f32 v43, v165, v43
	s_nop 0
	v_mfma_f32_32x32x16_f16 a[16:31], v[40:43], v[68:71], a[16:31]
	ds_read_b128 v[68:71], v74 offset:8704
	ds_read_b128 v[160:163], v74 offset:8736
	s_waitcnt lgkmcnt(1)
	v_mfma_f32_32x32x16_f16 a[0:15], v[60:63], v[68:71], 0
	v_mfma_f32_32x32x16_f16 a[0:15], v[40:43], v[68:71], a[0:15]
	v_mov_b32_e32 v40, 0x4400
	v_mad_u32_u24 v41, v76, s4, v40
	v_add_u32_e32 v40, v41, v72
	ds_read_b128 v[68:71], v40
	ds_read_b128 v[164:167], v40 offset:32
	s_waitcnt vmcnt(18)
	v_mul_f32_e32 v42, 0x43800000, v52
	v_mul_f32_e32 v43, 0x43800000, v53
	s_waitcnt lgkmcnt(1)
	v_mfma_f32_32x32x16_f16 a[16:31], v[60:63], v[68:71], a[16:31]
	ds_read_b128 v[68:71], v40 offset:8704
	ds_read_b128 v[168:171], v40 offset:8736
	s_waitcnt lgkmcnt(1)
	v_mfma_f32_32x32x16_f16 a[0:15], v[60:63], v[68:71], a[0:15]
	v_mul_f32_e32 v61, 0x43800000, v54
	v_mul_f32_e32 v62, 0x43800000, v55
	v_cvt_pk_f16_f32 v60, v42, v43
	v_cvt_pk_f16_f32 v61, v61, v62
	s_nop 0
	v_fma_mix_f32 v42, v52, s3, -v60 op_sel_hi:[0,0,1]
	v_fma_mix_f32 v43, v53, s3, -v60 op_sel:[0,0,1] op_sel_hi:[0,0,1]
	v_fma_mix_f32 v52, v54, s3, -v61 op_sel_hi:[0,0,1]
	v_fma_mix_f32 v53, v55, s3, -v61 op_sel:[0,0,1] op_sel_hi:[0,0,1]
	s_waitcnt vmcnt(17)
	v_mul_f32_e32 v54, 0x43800000, v48
	v_mul_f32_e32 v55, 0x43800000, v49
	v_cvt_pk_f16_f32 v62, v54, v55
	v_mul_f32_e32 v54, 0x43800000, v50
	v_mul_f32_e32 v55, 0x43800000, v51
	v_cvt_pk_f16_f32 v63, v54, v55
	v_fma_mix_f32 v54, v48, s3, -v62 op_sel_hi:[0,0,1]
	v_mfma_f32_32x32x16_f16 a[16:31], v[60:63], v[64:67], a[16:31]
	v_fma_mix_f32 v51, v51, s3, -v63 op_sel:[0,0,1] op_sel_hi:[0,0,1]
	v_fma_mix_f32 v55, v49, s3, -v62 op_sel:[0,0,1] op_sel_hi:[0,0,1]
	v_fma_mix_f32 v68, v50, s3, -v63 op_sel_hi:[0,0,1]
	v_cvt_pk_f16_f32 v48, v42, v43
	v_cvt_pk_f16_f32 v49, v52, v53
	v_cvt_pk_f16_f32 v50, v54, v55
	v_cvt_pk_f16_f32 v51, v68, v51
	v_mfma_f32_32x32x16_f16 a[0:15], v[60:63], v[160:163], a[0:15]
	ds_read_b128 v[52:55], v74 offset:64
	s_waitcnt vmcnt(14)
	v_mul_f32_e32 v42, 0x43800000, v56
	v_mul_f32_e32 v43, 0x43800000, v57
	v_mfma_f32_32x32x16_f16 a[16:31], v[48:51], v[64:67], a[16:31]
	v_mfma_f32_32x32x16_f16 a[0:15], v[48:51], v[160:163], a[0:15]
	v_mul_f32_e32 v49, 0x43800000, v58
	v_mul_f32_e32 v50, 0x43800000, v59
	v_cvt_pk_f16_f32 v49, v49, v50
	v_mul_f32_e32 v50, 0x43800000, v44
	v_mul_f32_e32 v51, 0x43800000, v45
	v_cvt_pk_f16_f32 v48, v42, v43
	v_cvt_pk_f16_f32 v50, v50, v51
	v_mfma_f32_32x32x16_f16 a[16:31], v[60:63], v[164:167], a[16:31]
	v_fma_mix_f32 v42, v56, s3, -v48 op_sel_hi:[0,0,1]
	v_mul_f32_e32 v51, 0x43800000, v46
	v_mul_f32_e32 v56, 0x43800000, v47
	v_fma_mix_f32 v43, v57, s3, -v48 op_sel:[0,0,1] op_sel_hi:[0,0,1]
	v_cvt_pk_f16_f32 v51, v51, v56
	v_fma_mix_f32 v44, v44, s3, -v50 op_sel_hi:[0,0,1]
	v_fma_mix_f32 v45, v45, s3, -v50 op_sel:[0,0,1] op_sel_hi:[0,0,1]
	s_waitcnt lgkmcnt(1)
	v_mfma_f32_32x32x16_f16 a[0:15], v[60:63], v[168:171], a[0:15]
	v_fma_mix_f32 v60, v58, s3, -v49 op_sel_hi:[0,0,1]
	v_fma_mix_f32 v61, v59, s3, -v49 op_sel:[0,0,1] op_sel_hi:[0,0,1]
	ds_read_b128 v[56:59], v74 offset:96
	v_fma_mix_f32 v46, v46, s3, -v51 op_sel_hi:[0,0,1]
	v_fma_mix_f32 v47, v47, s3, -v51 op_sel:[0,0,1] op_sel_hi:[0,0,1]
	v_cvt_pk_f16_f32 v42, v42, v43
	v_cvt_pk_f16_f32 v43, v60, v61
	s_waitcnt lgkmcnt(1)
	v_mfma_f32_32x32x16_f16 a[16:31], v[48:51], v[52:55], a[16:31]
	v_cvt_pk_f16_f32 v44, v44, v45
	v_cvt_pk_f16_f32 v45, v46, v47
	s_waitcnt vmcnt(13)
	v_mul_f32_e32 v46, 0x43800000, v3
	v_mfma_f32_32x32x16_f16 a[16:31], v[42:45], v[52:55], a[16:31]
	ds_read_b128 v[52:55], v74 offset:8768
	ds_read_b128 v[60:63], v74 offset:8800
	s_waitcnt lgkmcnt(1)
	v_mfma_f32_32x32x16_f16 a[0:15], v[48:51], v[52:55], a[0:15]
	v_mfma_f32_32x32x16_f16 a[0:15], v[42:45], v[52:55], a[0:15]
	ds_read_b128 v[42:45], v40 offset:64
	ds_read_b128 v[52:55], v40 offset:96
	s_waitcnt lgkmcnt(1)
	v_mfma_f32_32x32x16_f16 a[16:31], v[48:51], v[42:45], a[16:31]
	ds_read_b128 v[42:45], v40 offset:8768
	ds_read_b128 v[64:67], v40 offset:8800
	s_waitcnt lgkmcnt(1)
	v_mfma_f32_32x32x16_f16 a[0:15], v[48:51], v[42:45], a[0:15]
	s_waitcnt vmcnt(12)
	v_mul_f32_e32 v42, 0x43800000, v8
	v_mul_f32_e32 v43, 0x43800000, v9
	v_mul_f32_e32 v44, 0x43800000, v10
	v_mul_f32_e32 v45, 0x43800000, v11
	v_cvt_pk_f16_f32 v42, v42, v43
	v_cvt_pk_f16_f32 v43, v44, v45
	v_mul_f32_e32 v44, 0x43800000, v0
	v_mul_f32_e32 v45, 0x43800000, v1
	v_cvt_pk_f16_f32 v44, v44, v45
	v_mul_f32_e32 v45, 0x43800000, v2
	v_cvt_pk_f16_f32 v45, v45, v46
	v_fma_mix_f32 v8, v8, s3, -v42 op_sel_hi:[0,0,1]
	v_fma_mix_f32 v3, v3, s3, -v45 op_sel:[0,0,1] op_sel_hi:[0,0,1]
	v_mfma_f32_32x32x16_f16 a[16:31], v[42:45], v[56:59], a[16:31]
	v_fma_mix_f32 v9, v9, s3, -v42 op_sel:[0,0,1] op_sel_hi:[0,0,1]
	v_fma_mix_f32 v10, v10, s3, -v43 op_sel_hi:[0,0,1]
	v_fma_mix_f32 v11, v11, s3, -v43 op_sel:[0,0,1] op_sel_hi:[0,0,1]
	v_fma_mix_f32 v46, v0, s3, -v44 op_sel_hi:[0,0,1]
	v_fma_mix_f32 v47, v1, s3, -v44 op_sel:[0,0,1] op_sel_hi:[0,0,1]
	v_fma_mix_f32 v48, v2, s3, -v45 op_sel_hi:[0,0,1]
	v_cvt_pk_f16_f32 v0, v8, v9
	v_cvt_pk_f16_f32 v1, v10, v11
	v_cvt_pk_f16_f32 v2, v46, v47
	v_cvt_pk_f16_f32 v3, v48, v3
	s_waitcnt vmcnt(10)
	v_mul_f32_e32 v8, 0x43800000, v12
	v_mfma_f32_32x32x16_f16 a[16:31], v[0:3], v[56:59], a[16:31]
	v_mul_f32_e32 v9, 0x43800000, v13
	v_mul_f32_e32 v10, 0x43800000, v14
	v_mul_f32_e32 v11, 0x43800000, v15
	v_cvt_pk_f16_f32 v8, v8, v9
	v_cvt_pk_f16_f32 v9, v10, v11
	v_mul_f32_e32 v10, 0x43800000, v4
	v_fma_mix_f32 v50, v12, s3, -v8 op_sel_hi:[0,0,1]
	v_mfma_f32_32x32x16_f16 a[16:31], v[42:45], v[52:55], a[16:31]
	v_fma_mix_f32 v51, v13, s3, -v8 op_sel:[0,0,1] op_sel_hi:[0,0,1]
	v_fma_mix_f32 v52, v14, s3, -v9 op_sel_hi:[0,0,1]
	v_fma_mix_f32 v53, v15, s3, -v9 op_sel:[0,0,1] op_sel_hi:[0,0,1]
	ds_read_b128 v[12:15], v74 offset:128
	v_mul_f32_e32 v11, 0x43800000, v5
	v_cvt_pk_f16_f32 v10, v10, v11
	v_mul_f32_e32 v11, 0x43800000, v6
	v_mul_f32_e32 v46, 0x43800000, v7
	v_cvt_pk_f16_f32 v11, v11, v46
	ds_read_b128 v[46:49], v74 offset:160
	s_waitcnt lgkmcnt(1)
	v_mfma_f32_32x32x16_f16 a[16:31], v[8:11], v[12:15], a[16:31]
	v_fma_mix_f32 v7, v7, s3, -v11 op_sel:[0,0,1] op_sel_hi:[0,0,1]
	v_fma_mix_f32 v54, v4, s3, -v10 op_sel_hi:[0,0,1]
	v_fma_mix_f32 v55, v5, s3, -v10 op_sel:[0,0,1] op_sel_hi:[0,0,1]
	v_fma_mix_f32 v56, v6, s3, -v11 op_sel_hi:[0,0,1]
	v_cvt_pk_f16_f32 v4, v50, v51
	v_cvt_pk_f16_f32 v5, v52, v53
	v_cvt_pk_f16_f32 v6, v54, v55
	v_cvt_pk_f16_f32 v7, v56, v7
	s_waitcnt vmcnt(5)
	v_mul_f32_e32 v54, 0x43800000, v35
	v_mfma_f32_32x32x16_f16 a[16:31], v[4:7], v[12:15], a[16:31]
	ds_read_b128 v[12:15], v40 offset:128
	ds_read_b128 v[50:53], v40 offset:160
	v_mul_f32_e32 v57, 0x43800000, v135
	s_waitcnt lgkmcnt(1)
	v_mfma_f32_32x32x16_f16 a[16:31], v[8:11], v[12:15], a[16:31]
	s_waitcnt vmcnt(4)
	v_mul_f32_e32 v12, 0x43800000, v36
	v_mul_f32_e32 v13, 0x43800000, v37
	v_mul_f32_e32 v14, 0x43800000, v38
	v_mul_f32_e32 v15, 0x43800000, v39
	v_cvt_pk_f16_f32 v12, v12, v13
	v_cvt_pk_f16_f32 v13, v14, v15
	v_mul_f32_e32 v14, 0x43800000, v32
	v_mul_f32_e32 v15, 0x43800000, v33
	v_cvt_pk_f16_f32 v14, v14, v15
	v_mul_f32_e32 v15, 0x43800000, v34
	v_cvt_pk_f16_f32 v15, v15, v54
	v_fma_mix_f32 v36, v36, s3, -v12 op_sel_hi:[0,0,1]
	v_fma_mix_f32 v35, v35, s3, -v15 op_sel:[0,0,1] op_sel_hi:[0,0,1]
	v_mfma_f32_32x32x16_f16 a[16:31], v[12:15], v[46:49], a[16:31]
	v_fma_mix_f32 v37, v37, s3, -v12 op_sel:[0,0,1] op_sel_hi:[0,0,1]
	v_fma_mix_f32 v38, v38, s3, -v13 op_sel_hi:[0,0,1]
	v_fma_mix_f32 v39, v39, s3, -v13 op_sel:[0,0,1] op_sel_hi:[0,0,1]
	v_fma_mix_f32 v54, v32, s3, -v14 op_sel_hi:[0,0,1]
	v_fma_mix_f32 v55, v33, s3, -v14 op_sel:[0,0,1] op_sel_hi:[0,0,1]
	v_fma_mix_f32 v56, v34, s3, -v15 op_sel_hi:[0,0,1]
	v_cvt_pk_f16_f32 v32, v36, v37
	v_cvt_pk_f16_f32 v33, v38, v39
	v_cvt_pk_f16_f32 v34, v54, v55
	v_cvt_pk_f16_f32 v35, v56, v35
	s_waitcnt vmcnt(2)
	v_mul_f32_e32 v36, 0x43800000, v28
	v_mfma_f32_32x32x16_f16 a[16:31], v[32:35], v[46:49], a[16:31]
	v_mul_f32_e32 v37, 0x43800000, v29
	v_mul_f32_e32 v38, 0x43800000, v30
	v_mul_f32_e32 v39, 0x43800000, v31
	v_cvt_pk_f16_f32 v36, v36, v37
	v_cvt_pk_f16_f32 v37, v38, v39
	v_mul_f32_e32 v38, 0x43800000, v24
	v_mul_f32_e32 v39, 0x43800000, v25
	s_waitcnt lgkmcnt(0)
	v_mfma_f32_32x32x16_f16 a[16:31], v[12:15], v[50:53], a[16:31]
	v_fma_mix_f32 v50, v28, s3, -v36 op_sel_hi:[0,0,1]
	v_fma_mix_f32 v51, v29, s3, -v36 op_sel:[0,0,1] op_sel_hi:[0,0,1]
	v_fma_mix_f32 v52, v30, s3, -v37 op_sel_hi:[0,0,1]
	v_fma_mix_f32 v53, v31, s3, -v37 op_sel:[0,0,1] op_sel_hi:[0,0,1]
	ds_read_b128 v[28:31], v74 offset:192
	v_cvt_pk_f16_f32 v38, v38, v39
	v_mul_f32_e32 v39, 0x43800000, v26
	v_mul_f32_e32 v46, 0x43800000, v27
	v_mfma_f32_32x32x16_f16 a[0:15], v[42:45], v[60:63], a[0:15]
	v_cvt_pk_f16_f32 v39, v39, v46
	ds_read_b128 v[46:49], v74 offset:224
	v_fma_mix_f32 v27, v27, s3, -v39 op_sel:[0,0,1] op_sel_hi:[0,0,1]
	v_fma_mix_f32 v54, v24, s3, -v38 op_sel_hi:[0,0,1]
	v_fma_mix_f32 v55, v25, s3, -v38 op_sel:[0,0,1] op_sel_hi:[0,0,1]
	v_fma_mix_f32 v56, v26, s3, -v39 op_sel_hi:[0,0,1]
	v_cvt_pk_f16_f32 v24, v50, v51
	s_waitcnt lgkmcnt(1)
	v_mfma_f32_32x32x16_f16 a[16:31], v[36:39], v[28:31], a[16:31]
	v_cvt_pk_f16_f32 v25, v52, v53
	v_cvt_pk_f16_f32 v26, v54, v55
	v_cvt_pk_f16_f32 v27, v56, v27
	s_waitcnt vmcnt(1)
	v_mul_f32_e32 v54, 0x43800000, v19
	v_mfma_f32_32x32x16_f16 a[0:15], v[0:3], v[60:63], a[0:15]
	v_mfma_f32_32x32x16_f16 a[16:31], v[24:27], v[28:31], a[16:31]
	ds_read_b128 v[28:31], v40 offset:192
	ds_read_b128 v[50:53], v40 offset:224
	v_mfma_f32_32x32x16_f16 a[0:15], v[42:45], v[64:67], a[0:15]
	v_mov_b32_e32 v44, v158
	v_mov_b32_e32 v42, v159
	s_waitcnt lgkmcnt(1)
	v_mfma_f32_32x32x16_f16 a[16:31], v[36:39], v[28:31], a[16:31]
	s_waitcnt vmcnt(0)
	v_mul_f32_e32 v28, 0x43800000, v20
	v_mul_f32_e32 v29, 0x43800000, v21
	v_mul_f32_e32 v30, 0x43800000, v22
	v_mul_f32_e32 v31, 0x43800000, v23
	v_cvt_pk_f16_f32 v28, v28, v29
	v_cvt_pk_f16_f32 v29, v30, v31
	v_mul_f32_e32 v30, 0x43800000, v16
	v_mul_f32_e32 v31, 0x43800000, v17
	v_fma_mix_f32 v20, v20, s3, -v28 op_sel_hi:[0,0,1]
	v_fma_mix_f32 v21, v21, s3, -v28 op_sel:[0,0,1] op_sel_hi:[0,0,1]
	v_fma_mix_f32 v22, v22, s3, -v29 op_sel_hi:[0,0,1]
	v_fma_mix_f32 v23, v23, s3, -v29 op_sel:[0,0,1] op_sel_hi:[0,0,1]
	v_cvt_pk_f16_f32 v30, v30, v31
	v_mul_f32_e32 v31, 0x43800000, v18
	v_cvt_pk_f16_f32 v31, v31, v54
	v_fma_mix_f32 v54, v16, s3, -v30 op_sel_hi:[0,0,1]
	v_fma_mix_f32 v55, v17, s3, -v30 op_sel:[0,0,1] op_sel_hi:[0,0,1]
	v_cvt_pk_f16_f32 v16, v20, v21
	v_cvt_pk_f16_f32 v17, v22, v23
	ds_read_b128 v[0:3], v74 offset:8832
	ds_read_b128 v[20:23], v74 offset:8864
	s_waitcnt lgkmcnt(1)
	v_mfma_f32_32x32x16_f16 a[0:15], v[8:11], v[0:3], a[0:15]
	v_fma_mix_f32 v19, v19, s3, -v31 op_sel:[0,0,1] op_sel_hi:[0,0,1]
	v_fma_mix_f32 v56, v18, s3, -v31 op_sel_hi:[0,0,1]
	v_cvt_pk_f16_f32 v18, v54, v55
	v_cvt_pk_f16_f32 v19, v56, v19
	v_mul_f32_e32 v54, 0x43800000, v139
	v_mul_f32_e32 v55, 0x43800000, v133
	v_mul_f32_e32 v56, 0x43800000, v134
	v_mfma_f32_32x32x16_f16 a[0:15], v[4:7], v[0:3], a[0:15]
	ds_read_b128 v[0:3], v40 offset:8832
	ds_read_b128 v[4:7], v40 offset:8864
	s_waitcnt lgkmcnt(1)
	v_mfma_f32_32x32x16_f16 a[0:15], v[8:11], v[0:3], a[0:15]
	ds_read_b128 v[0:3], v74 offset:8896
	ds_read_b128 v[8:11], v74 offset:8928
	v_mfma_f32_32x32x16_f16 a[0:15], v[12:15], v[20:23], a[0:15]
	v_mfma_f32_32x32x16_f16 a[0:15], v[32:35], v[20:23], a[0:15]
	v_mov_b32_e32 v32, v155
	v_mov_b32_e32 v34, v154
	s_waitcnt lgkmcnt(2)
	v_mfma_f32_32x32x16_f16 a[0:15], v[12:15], v[4:7], a[0:15]
	ds_read_b128 v[12:15], v40 offset:8896
	ds_read_b128 v[20:23], v40 offset:8928
	s_waitcnt lgkmcnt(0)
	s_barrier
	v_mfma_f32_32x32x16_f16 a[0:15], v[36:39], v[0:3], a[0:15]
	v_mfma_f32_32x32x16_f16 a[0:15], v[24:27], v[0:3], a[0:15]
	v_mov_b32_e32 v26, v148
	v_mov_b32_e32 v24, v149
	v_mfma_f32_32x32x16_f16 a[0:15], v[36:39], v[12:15], a[0:15]
	v_mov_b32_e32 v38, v152
	v_mov_b32_e32 v36, v153
	v_mfma_f32_32x32x16_f16 a[16:31], v[28:31], v[46:49], a[16:31]
	v_mfma_f32_32x32x16_f16 a[0:15], v[28:31], v[8:11], a[0:15]
	v_mfma_f32_32x32x16_f16 a[16:31], v[16:19], v[46:49], a[16:31]
	v_mov_b32_e32 v48, v156
	v_mov_b32_e32 v46, v157
	v_mfma_f32_32x32x16_f16 a[0:15], v[16:19], v[8:11], a[0:15]
	v_mfma_f32_32x32x16_f16 a[16:31], v[28:31], v[50:53], a[16:31]
	v_mul_f32_e32 v50, 0x43800000, v140
	v_mul_f32_e32 v51, 0x43800000, v136
	v_mul_f32_e32 v52, 0x43800000, v137
	v_mul_f32_e32 v53, 0x43800000, v138
	v_mfma_f32_32x32x16_f16 a[0:15], v[28:31], v[20:23], a[0:15]
	s_nop 6
	v_accvgpr_read_b32 v45, a18
	v_accvgpr_read_b32 v47, a17
	v_accvgpr_read_b32 v49, a16
	v_mul_f32_e64 v8, v48, s0
	v_mul_f32_e64 v9, v49, s1
	v_pk_mul_f32 v[10:11], v[46:47], s[0:1]
	v_pk_mul_f32 v[16:17], v[44:45], s[0:1]
	v_add_f32_e32 v0, v8, v9
	v_accvgpr_read_b32 v43, a19
	v_accvgpr_read_b32 v2, a0
	v_accvgpr_read_b32 v4, a1
	v_accvgpr_read_b32 v6, a2
	v_fmac_f32_e32 v8, 0x3b800000, v2
	v_add_f32_e32 v2, v10, v11
	v_fmac_f32_e32 v10, 0x3b800000, v4
	v_add_f32_e32 v4, v16, v17
	v_fmac_f32_e32 v16, 0x3b800000, v6
	v_cvt_pk_f16_f32 v20, v0, v2
	v_pk_mul_f32 v[18:19], v[42:43], s[0:1]
	v_cvt_f32_f16_e32 v6, v20
	v_cvt_f32_f16_sdwa v9, v20 dst_sel:DWORD dst_unused:UNUSED_PAD src0_sel:WORD_1
	v_add_f32_e32 v11, v18, v19
	v_cvt_pk_f16_f32 v21, v4, v11
	v_sub_f32_e32 v0, v0, v6
	v_cvt_f32_f16_e32 v6, v21
	v_sub_f32_e32 v2, v2, v9
	v_cvt_f32_f16_sdwa v9, v21 dst_sel:DWORD dst_unused:UNUSED_PAD src0_sel:WORD_1
	v_cvt_pk_f16_f32 v22, v0, v2
	v_accvgpr_read_b32 v2, a3
	v_sub_f32_e32 v4, v4, v6
	v_cvt_pk_f16_f32 v28, v8, v10
	v_fmac_f32_e32 v18, 0x3b800000, v2
	v_cvt_f32_f16_e32 v0, v28
	v_cvt_f32_f16_sdwa v2, v28 dst_sel:DWORD dst_unused:UNUSED_PAD src0_sel:WORD_1
	v_sub_f32_e32 v6, v11, v9
	v_cvt_pk_f16_f32 v23, v4, v6
	v_cvt_pk_f16_f32 v29, v16, v18
	v_accvgpr_read_b32 v37, a21
	v_cvt_f32_f16_e32 v4, v29
	v_accvgpr_read_b32 v39, a20
	v_sub_f32_e32 v0, v8, v0
	v_cvt_f32_f16_sdwa v6, v29 dst_sel:DWORD dst_unused:UNUSED_PAD src0_sel:WORD_1
	v_sub_f32_e32 v2, v10, v2
	v_accvgpr_read_b32 v33, a23
	v_sub_f32_e32 v4, v16, v4
	v_cvt_pk_f16_f32 v8, v0, v2
	v_lshlrev_b32_e32 v0, 1, v142
	v_pk_mul_f32 v[10:11], v[38:39], s[0:1]
	v_accvgpr_read_b32 v2, a4
	v_pk_mul_f32 v[16:17], v[36:37], s[0:1]
	v_lshl_or_b32 v72, v141, 3, v0
	v_add_f32_e32 v0, v10, v11
	v_fmac_f32_e32 v10, 0x3b800000, v2
	v_add_f32_e32 v2, v16, v17
	v_pk_mul_f32 v[30:31], v[32:33], s[0:1]
	v_cvt_pk_f16_f32 v32, v0, v2
	v_accvgpr_read_b32 v35, a22
	v_cvt_f32_f16_e32 v11, v32
	v_sub_f32_e32 v6, v18, v6
	v_cvt_pk_f16_f32 v9, v4, v6
	v_accvgpr_read_b32 v4, a5
	v_pk_mul_f32 v[18:19], v[34:35], s[0:1]
	v_accvgpr_read_b32 v6, a6
	v_accvgpr_read_b32 v12, a7
	v_fmac_f32_e32 v16, 0x3b800000, v4
	v_add_f32_e32 v4, v18, v19
	v_fmac_f32_e32 v18, 0x3b800000, v6
	v_add_f32_e32 v6, v30, v31
	v_fmac_f32_e32 v30, 0x3b800000, v12
	v_cvt_pk_f16_f32 v33, v4, v6
	v_sub_f32_e32 v0, v0, v11
	v_cvt_f32_f16_sdwa v11, v32 dst_sel:DWORD dst_unused:UNUSED_PAD src0_sel:WORD_1
	v_cvt_f32_f16_e32 v12, v33
	v_cvt_f32_f16_sdwa v14, v33 dst_sel:DWORD dst_unused:UNUSED_PAD src0_sel:WORD_1
	v_cvt_pk_f16_f32 v34, v10, v16
	v_sub_f32_e32 v2, v2, v11
	v_sub_f32_e32 v4, v4, v12
	v_sub_f32_e32 v6, v6, v14
	v_cvt_f32_f16_e32 v11, v34
	v_cvt_pk_f16_f32 v36, v0, v2
	v_cvt_pk_f16_f32 v37, v4, v6
	v_cvt_pk_f16_f32 v35, v18, v30
	v_cvt_f32_f16_sdwa v2, v34 dst_sel:DWORD dst_unused:UNUSED_PAD src0_sel:WORD_1
	v_cvt_f32_f16_e32 v4, v35
	v_cvt_f32_f16_sdwa v6, v35 dst_sel:DWORD dst_unused:UNUSED_PAD src0_sel:WORD_1
	v_mad_u32_u24 v31, v76, s4, v72
	v_add_u32_e32 v38, v41, v72
	v_accvgpr_read_b32 v13, a27
	v_accvgpr_read_b32 v15, a26
	v_accvgpr_read_b32 v25, a25
	v_accvgpr_read_b32 v27, a24
	v_sub_f32_e32 v0, v10, v11
	v_sub_f32_e32 v2, v16, v2
	v_sub_f32_e32 v4, v18, v4
	v_sub_f32_e32 v6, v30, v6
	v_cvt_pk_f16_f32 v10, v0, v2
	v_cvt_pk_f16_f32 v11, v4, v6
	ds_write2_b64 v31, v[20:21], v[32:33] offset1:2
	ds_write2_b64 v38, v[22:23], v[36:37] offset1:2
	v_add_u32_e32 v23, 0x2000, v38
	v_mov_b32_e32 v14, v150
	v_mov_b32_e32 v12, v151
	ds_write2_b64 v23, v[8:9], v[10:11] offset0:64 offset1:66
	v_pk_mul_f32 v[8:9], v[26:27], s[0:1]
	v_accvgpr_read_b32 v2, a8
	v_pk_mul_f32 v[10:11], v[24:25], s[0:1]
	v_accvgpr_read_b32 v4, a9
	v_pk_mul_f32 v[14:15], v[14:15], s[0:1]
	v_accvgpr_read_b32 v6, a10
	v_pk_mul_f32 v[12:13], v[12:13], s[0:1]
	v_add_f32_e32 v0, v8, v9
	v_fmac_f32_e32 v8, 0x3b800000, v2
	v_add_f32_e32 v2, v10, v11
	v_fmac_f32_e32 v10, 0x3b800000, v4
	v_add_f32_e32 v4, v14, v15
	v_fmac_f32_e32 v14, 0x3b800000, v6
	v_add_f32_e32 v6, v12, v13
	v_accvgpr_read_b32 v9, a11
	v_cvt_pk_f16_f32 v17, v4, v6
	v_fmac_f32_e32 v12, 0x3b800000, v9
	v_cvt_f32_f16_sdwa v15, v17 dst_sel:DWORD dst_unused:UNUSED_PAD src0_sel:WORD_1
	v_cvt_pk_f16_f32 v16, v0, v2
	v_cvt_f32_f16_e32 v13, v17
	v_cvt_f32_f16_e32 v9, v16
	v_cvt_f32_f16_sdwa v11, v16 dst_sel:DWORD dst_unused:UNUSED_PAD src0_sel:WORD_1
	v_sub_f32_e32 v6, v6, v15
	v_sub_f32_e32 v4, v4, v13
	v_sub_f32_e32 v0, v0, v9
	v_cvt_pk_f16_f32 v19, v4, v6
	v_cvt_pk_f16_f32 v21, v14, v12
	v_sub_f32_e32 v2, v2, v11
	v_cvt_f32_f16_sdwa v6, v21 dst_sel:DWORD dst_unused:UNUSED_PAD src0_sel:WORD_1
	v_cvt_pk_f16_f32 v18, v0, v2
	v_cvt_pk_f16_f32 v20, v8, v10
	v_cvt_f32_f16_e32 v4, v21
	v_cvt_f32_f16_e32 v0, v20
	v_cvt_f32_f16_sdwa v2, v20 dst_sel:DWORD dst_unused:UNUSED_PAD src0_sel:WORD_1
	v_sub_f32_e32 v6, v12, v6
	v_accvgpr_read_b32 v7, a28
	v_sub_f32_e32 v0, v8, v0
	v_sub_f32_e32 v4, v14, v4
	v_cvt_pk_f16_f32 v9, v4, v6
	v_mov_b32_e32 v6, v144
	v_accvgpr_read_b32 v5, a29
	v_sub_f32_e32 v2, v10, v2
	v_cvt_pk_f16_f32 v8, v0, v2
	v_pk_mul_f32 v[6:7], v[6:7], s[0:1]
	v_accvgpr_read_b32 v0, a12
	v_mov_b32_e32 v4, v145
	v_accvgpr_read_b32 v3, a30
	v_add_f32_e32 v7, v6, v7
	v_fmac_f32_e32 v6, 0x3b800000, v0
	v_pk_mul_f32 v[4:5], v[4:5], s[0:1]
	v_accvgpr_read_b32 v0, a13
	v_mov_b32_e32 v2, v146
	v_add_f32_e32 v5, v4, v5
	v_fmac_f32_e32 v4, 0x3b800000, v0
	v_pk_mul_f32 v[2:3], v[2:3], s[0:1]
	v_accvgpr_read_b32 v0, a14
	v_accvgpr_read_b32 v1, a31
	v_add_f32_e32 v3, v2, v3
	v_fmac_f32_e32 v2, 0x3b800000, v0
	v_mov_b32_e32 v0, v147
	v_pk_mul_f32 v[0:1], v[0:1], s[0:1]
	v_accvgpr_read_b32 v10, a15
	v_add_f32_e32 v1, v0, v1
	v_cvt_pk_f16_f32 v11, v3, v1
	v_fmac_f32_e32 v0, 0x3b800000, v10
	v_cvt_f32_f16_sdwa v15, v11 dst_sel:DWORD dst_unused:UNUSED_PAD src0_sel:WORD_1
	v_cvt_pk_f16_f32 v10, v7, v5
	v_cvt_f32_f16_e32 v14, v11
	v_cvt_f32_f16_e32 v12, v10
	v_cvt_f32_f16_sdwa v13, v10 dst_sel:DWORD dst_unused:UNUSED_PAD src0_sel:WORD_1
	v_sub_f32_e32 v1, v1, v15
	v_sub_f32_e32 v3, v3, v14
	v_sub_f32_e32 v7, v7, v12
	v_sub_f32_e32 v5, v5, v13
	v_cvt_pk_f16_f32 v13, v3, v1
	v_cvt_pk_f16_f32 v14, v6, v4
	v_cvt_pk_f16_f32 v12, v7, v5
	v_cvt_pk_f16_f32 v15, v2, v0
	v_add_u32_e32 v22, 0x2000, v31
	v_cvt_f32_f16_e32 v1, v14
	v_cvt_f32_f16_sdwa v3, v14 dst_sel:DWORD dst_unused:UNUSED_PAD src0_sel:WORD_1
	v_cvt_f32_f16_e32 v5, v15
	v_cvt_f32_f16_sdwa v7, v15 dst_sel:DWORD dst_unused:UNUSED_PAD src0_sel:WORD_1
	v_sub_f32_e32 v1, v6, v1
	v_sub_f32_e32 v3, v4, v3
	v_sub_f32_e32 v2, v2, v5
	v_sub_f32_e32 v4, v0, v7
	v_cvt_pk_f16_f32 v0, v1, v3
	v_cvt_pk_f16_f32 v1, v2, v4
	ds_write2_b64 v22, v[28:29], v[34:35] offset0:64 offset1:66
	ds_write2_b64 v31, v[16:17], v[10:11] offset0:4 offset1:6
	ds_write2_b64 v38, v[18:19], v[12:13] offset0:4 offset1:6
	ds_write2_b64 v22, v[20:21], v[14:15] offset0:68 offset1:70
	ds_write2_b64 v23, v[8:9], v[0:1] offset0:68 offset1:70
	s_waitcnt lgkmcnt(0)
	s_barrier
	ds_read_b128 v[0:3], v74
	ds_read_b128 v[8:11], v74 offset:32
	ds_read_b128 v[12:15], v74 offset:8704
	ds_read_b128 v[16:19], v74 offset:8736
	v_cvt_pk_f16_f32 v4, v50, v51
	v_cvt_pk_f16_f32 v5, v52, v53
	v_cvt_pk_f16_f32 v6, v54, v55
	v_cvt_pk_f16_f32 v7, v56, v57
	v_mul_f32_e32 v28, 0x43800000, v124
	s_waitcnt lgkmcnt(3)
	v_mfma_f32_32x32x16_f16 a[0:15], v[4:7], v[0:3], 0
	v_fma_mix_f32 v20, v140, s3, -v4 op_sel_hi:[0,0,1]
	v_fma_mix_f32 v21, v136, s3, -v4 op_sel:[0,0,1] op_sel_hi:[0,0,1]
	v_fma_mix_f32 v22, v137, s3, -v5 op_sel_hi:[0,0,1]
	v_fma_mix_f32 v23, v138, s3, -v5 op_sel:[0,0,1] op_sel_hi:[0,0,1]
	v_fma_mix_f32 v24, v139, s3, -v6 op_sel_hi:[0,0,1]
	v_fma_mix_f32 v25, v133, s3, -v6 op_sel:[0,0,1] op_sel_hi:[0,0,1]
	v_fma_mix_f32 v26, v134, s3, -v7 op_sel_hi:[0,0,1]
	s_waitcnt lgkmcnt(1)
	v_mfma_f32_32x32x16_f16 a[16:31], v[4:7], v[12:15], 0
	v_fma_mix_f32 v27, v135, s3, -v7 op_sel:[0,0,1] op_sel_hi:[0,0,1]
	v_cvt_pk_f16_f32 v20, v20, v21
	v_cvt_pk_f16_f32 v21, v22, v23
	v_cvt_pk_f16_f32 v22, v24, v25
	v_cvt_pk_f16_f32 v23, v26, v27
	v_mul_f32_e32 v24, 0x43800000, v120
	v_mul_f32_e32 v25, 0x43800000, v121
	v_mfma_f32_32x32x16_f16 a[0:15], v[20:23], v[0:3], a[0:15]
	v_mul_f32_e32 v26, 0x43800000, v122
	v_mul_f32_e32 v27, 0x43800000, v123
	s_mov_b64 s[0:1], 0x2000
	v_mfma_f32_32x32x16_f16 a[16:31], v[20:23], v[12:15], a[16:31]
	ds_read_b128 v[0:3], v40
	ds_read_b128 v[12:15], v40 offset:32
	ds_read_b128 v[20:23], v40 offset:8736
	s_waitcnt lgkmcnt(2)
	v_mfma_f32_32x32x16_f16 a[0:15], v[4:7], v[0:3], a[0:15]
	ds_read_b128 v[0:3], v40 offset:8704
	s_waitcnt lgkmcnt(0)
	v_mfma_f32_32x32x16_f16 a[16:31], v[4:7], v[0:3], a[16:31]
	v_mul_f32_e32 v2, 0x43800000, v117
	v_mul_f32_e32 v3, 0x43800000, v118
	v_mul_f32_e32 v4, 0x43800000, v119
	v_cvt_pk_f16_f32 v0, v24, v25
	v_cvt_pk_f16_f32 v1, v26, v27
	v_cvt_pk_f16_f32 v2, v28, v2
	v_cvt_pk_f16_f32 v3, v3, v4
	v_mul_f32_e32 v28, 0x43800000, v116
	v_mfma_f32_32x32x16_f16 a[0:15], v[0:3], v[8:11], a[0:15]
	v_fma_mix_f32 v4, v120, s3, -v0 op_sel_hi:[0,0,1]
	v_fma_mix_f32 v5, v121, s3, -v0 op_sel:[0,0,1] op_sel_hi:[0,0,1]
	v_fma_mix_f32 v6, v122, s3, -v1 op_sel_hi:[0,0,1]
	v_fma_mix_f32 v7, v123, s3, -v1 op_sel:[0,0,1] op_sel_hi:[0,0,1]
	v_fma_mix_f32 v24, v124, s3, -v2 op_sel_hi:[0,0,1]
	v_fma_mix_f32 v25, v117, s3, -v2 op_sel:[0,0,1] op_sel_hi:[0,0,1]
	v_fma_mix_f32 v26, v118, s3, -v3 op_sel_hi:[0,0,1]
	v_mfma_f32_32x32x16_f16 a[16:31], v[0:3], v[16:19], a[16:31]
	v_fma_mix_f32 v27, v119, s3, -v3 op_sel:[0,0,1] op_sel_hi:[0,0,1]
	v_cvt_pk_f16_f32 v4, v4, v5
	v_cvt_pk_f16_f32 v5, v6, v7
	v_cvt_pk_f16_f32 v6, v24, v25
	v_cvt_pk_f16_f32 v7, v26, v27
	s_nop 0
	v_mfma_f32_32x32x16_f16 a[0:15], v[4:7], v[8:11], a[0:15]
	v_mul_f32_e32 v8, 0x43800000, v131
	v_mul_f32_e32 v9, 0x43800000, v125
	v_mul_f32_e32 v10, 0x43800000, v126
	v_mul_f32_e32 v11, 0x43800000, v127
	v_mfma_f32_32x32x16_f16 a[16:31], v[4:7], v[16:19], a[16:31]
	v_mul_f32_e32 v4, 0x43800000, v132
	v_mul_f32_e32 v5, 0x43800000, v128
	v_mul_f32_e32 v6, 0x43800000, v129
	v_mul_f32_e32 v7, 0x43800000, v130
	v_cvt_pk_f16_f32 v4, v4, v5
	v_cvt_pk_f16_f32 v5, v6, v7
	v_cvt_pk_f16_f32 v6, v8, v9
	v_mfma_f32_32x32x16_f16 a[0:15], v[0:3], v[12:15], a[0:15]
	ds_read_b128 v[12:15], v74 offset:8768
	ds_read_b128 v[16:19], v74 offset:8800
	v_cvt_pk_f16_f32 v7, v10, v11
	ds_read_b128 v[8:11], v74 offset:96
	v_fma_mix_f32 v24, v131, s3, -v6 op_sel_hi:[0,0,1]
	v_fma_mix_f32 v25, v125, s3, -v6 op_sel:[0,0,1] op_sel_hi:[0,0,1]
	v_fma_mix_f32 v26, v126, s3, -v7 op_sel_hi:[0,0,1]
	v_mfma_f32_32x32x16_f16 a[16:31], v[0:3], v[20:23], a[16:31]
	ds_read_b128 v[0:3], v74 offset:64
	v_fma_mix_f32 v20, v132, s3, -v4 op_sel_hi:[0,0,1]
	v_fma_mix_f32 v21, v128, s3, -v4 op_sel:[0,0,1] op_sel_hi:[0,0,1]
	v_fma_mix_f32 v22, v129, s3, -v5 op_sel_hi:[0,0,1]
	v_fma_mix_f32 v23, v130, s3, -v5 op_sel:[0,0,1] op_sel_hi:[0,0,1]
	v_fma_mix_f32 v27, v127, s3, -v7 op_sel:[0,0,1] op_sel_hi:[0,0,1]
	v_cvt_pk_f16_f32 v20, v20, v21
	s_waitcnt lgkmcnt(0)
	v_mfma_f32_32x32x16_f16 a[0:15], v[4:7], v[0:3], a[0:15]
	v_cvt_pk_f16_f32 v21, v22, v23
	v_cvt_pk_f16_f32 v22, v24, v25
	v_cvt_pk_f16_f32 v23, v26, v27
	v_mul_f32_e32 v24, 0x43800000, v112
	v_mul_f32_e32 v25, 0x43800000, v113
	v_mul_f32_e32 v26, 0x43800000, v114
	v_mul_f32_e32 v27, 0x43800000, v115
	v_mfma_f32_32x32x16_f16 a[16:31], v[4:7], v[12:15], a[16:31]
	v_mfma_f32_32x32x16_f16 a[0:15], v[20:23], v[0:3], a[0:15]
	v_mfma_f32_32x32x16_f16 a[16:31], v[20:23], v[12:15], a[16:31]
	ds_read_b128 v[0:3], v40 offset:64
	ds_read_b128 v[12:15], v40 offset:96
	ds_read_b128 v[20:23], v40 offset:8800
	s_waitcnt lgkmcnt(2)
	v_mfma_f32_32x32x16_f16 a[0:15], v[4:7], v[0:3], a[0:15]
	ds_read_b128 v[0:3], v40 offset:8768
	s_waitcnt lgkmcnt(0)
	v_mfma_f32_32x32x16_f16 a[16:31], v[4:7], v[0:3], a[16:31]
	v_mul_f32_e32 v2, 0x43800000, v109
	v_mul_f32_e32 v3, 0x43800000, v110
	v_mul_f32_e32 v4, 0x43800000, v111
	v_cvt_pk_f16_f32 v0, v24, v25
	v_cvt_pk_f16_f32 v1, v26, v27
	v_cvt_pk_f16_f32 v2, v28, v2
	v_cvt_pk_f16_f32 v3, v3, v4
	v_mul_f32_e32 v28, 0x43800000, v95
	v_mfma_f32_32x32x16_f16 a[0:15], v[0:3], v[8:11], a[0:15]
	v_fma_mix_f32 v4, v112, s3, -v0 op_sel_hi:[0,0,1]
	v_fma_mix_f32 v5, v113, s3, -v0 op_sel:[0,0,1] op_sel_hi:[0,0,1]
	v_fma_mix_f32 v6, v114, s3, -v1 op_sel_hi:[0,0,1]
	v_fma_mix_f32 v7, v115, s3, -v1 op_sel:[0,0,1] op_sel_hi:[0,0,1]
	v_fma_mix_f32 v24, v116, s3, -v2 op_sel_hi:[0,0,1]
	v_fma_mix_f32 v25, v109, s3, -v2 op_sel:[0,0,1] op_sel_hi:[0,0,1]
	v_fma_mix_f32 v26, v110, s3, -v3 op_sel_hi:[0,0,1]
	v_mfma_f32_32x32x16_f16 a[16:31], v[0:3], v[16:19], a[16:31]
	v_fma_mix_f32 v27, v111, s3, -v3 op_sel:[0,0,1] op_sel_hi:[0,0,1]
	v_cvt_pk_f16_f32 v4, v4, v5
	v_cvt_pk_f16_f32 v5, v6, v7
	v_cvt_pk_f16_f32 v6, v24, v25
	v_cvt_pk_f16_f32 v7, v26, v27
	s_nop 0
	v_mfma_f32_32x32x16_f16 a[0:15], v[4:7], v[8:11], a[0:15]
	v_mul_f32_e32 v8, 0x43800000, v107
	v_mul_f32_e32 v9, 0x43800000, v101
	v_mul_f32_e32 v10, 0x43800000, v102
	v_mul_f32_e32 v11, 0x43800000, v103
	v_mfma_f32_32x32x16_f16 a[16:31], v[4:7], v[16:19], a[16:31]
	v_mul_f32_e32 v4, 0x43800000, v108
	v_mul_f32_e32 v5, 0x43800000, v104
	v_mul_f32_e32 v6, 0x43800000, v105
	v_mul_f32_e32 v7, 0x43800000, v106
	v_cvt_pk_f16_f32 v4, v4, v5
	v_cvt_pk_f16_f32 v5, v6, v7
	v_cvt_pk_f16_f32 v6, v8, v9
	v_mfma_f32_32x32x16_f16 a[0:15], v[0:3], v[12:15], a[0:15]
	ds_read_b128 v[12:15], v74 offset:8832
	ds_read_b128 v[16:19], v74 offset:8864
	v_cvt_pk_f16_f32 v7, v10, v11
	ds_read_b128 v[8:11], v74 offset:160
	v_fma_mix_f32 v24, v107, s3, -v6 op_sel_hi:[0,0,1]
	v_fma_mix_f32 v25, v101, s3, -v6 op_sel:[0,0,1] op_sel_hi:[0,0,1]
	v_fma_mix_f32 v26, v102, s3, -v7 op_sel_hi:[0,0,1]
	v_mfma_f32_32x32x16_f16 a[16:31], v[0:3], v[20:23], a[16:31]
	ds_read_b128 v[0:3], v74 offset:128
	v_fma_mix_f32 v20, v108, s3, -v4 op_sel_hi:[0,0,1]
	v_fma_mix_f32 v21, v104, s3, -v4 op_sel:[0,0,1] op_sel_hi:[0,0,1]
	v_fma_mix_f32 v22, v105, s3, -v5 op_sel_hi:[0,0,1]
	v_fma_mix_f32 v23, v106, s3, -v5 op_sel:[0,0,1] op_sel_hi:[0,0,1]
	v_fma_mix_f32 v27, v103, s3, -v7 op_sel:[0,0,1] op_sel_hi:[0,0,1]
	v_cvt_pk_f16_f32 v20, v20, v21
	s_waitcnt lgkmcnt(0)
	v_mfma_f32_32x32x16_f16 a[0:15], v[4:7], v[0:3], a[0:15]
	v_cvt_pk_f16_f32 v21, v22, v23
	v_cvt_pk_f16_f32 v22, v24, v25
	v_cvt_pk_f16_f32 v23, v26, v27
	v_mul_f32_e32 v24, 0x43800000, v91
	v_mul_f32_e32 v25, 0x43800000, v92
	v_mul_f32_e32 v26, 0x43800000, v93
	v_mul_f32_e32 v27, 0x43800000, v94
	v_mfma_f32_32x32x16_f16 a[16:31], v[4:7], v[12:15], a[16:31]
	v_mfma_f32_32x32x16_f16 a[0:15], v[20:23], v[0:3], a[0:15]
	v_mfma_f32_32x32x16_f16 a[16:31], v[20:23], v[12:15], a[16:31]
	ds_read_b128 v[0:3], v40 offset:128
	ds_read_b128 v[12:15], v40 offset:160
	ds_read_b128 v[20:23], v40 offset:8864
	s_waitcnt lgkmcnt(2)
	v_mfma_f32_32x32x16_f16 a[0:15], v[4:7], v[0:3], a[0:15]
	ds_read_b128 v[0:3], v40 offset:8832
	s_waitcnt lgkmcnt(0)
	v_mfma_f32_32x32x16_f16 a[16:31], v[4:7], v[0:3], a[16:31]
	v_mul_f32_e32 v2, 0x43800000, v88
	v_mul_f32_e32 v3, 0x43800000, v89
	v_mul_f32_e32 v4, 0x43800000, v90
	v_cvt_pk_f16_f32 v0, v24, v25
	v_cvt_pk_f16_f32 v1, v26, v27
	v_cvt_pk_f16_f32 v2, v28, v2
	v_cvt_pk_f16_f32 v3, v3, v4
	v_mul_f32_e32 v28, 0x43800000, v84
	v_mfma_f32_32x32x16_f16 a[0:15], v[0:3], v[8:11], a[0:15]
	v_fma_mix_f32 v4, v91, s3, -v0 op_sel_hi:[0,0,1]
	v_fma_mix_f32 v5, v92, s3, -v0 op_sel:[0,0,1] op_sel_hi:[0,0,1]
	v_fma_mix_f32 v6, v93, s3, -v1 op_sel_hi:[0,0,1]
	v_fma_mix_f32 v7, v94, s3, -v1 op_sel:[0,0,1] op_sel_hi:[0,0,1]
	v_fma_mix_f32 v24, v95, s3, -v2 op_sel_hi:[0,0,1]
	v_fma_mix_f32 v25, v88, s3, -v2 op_sel:[0,0,1] op_sel_hi:[0,0,1]
	v_fma_mix_f32 v26, v89, s3, -v3 op_sel_hi:[0,0,1]
	v_mfma_f32_32x32x16_f16 a[16:31], v[0:3], v[16:19], a[16:31]
	v_fma_mix_f32 v27, v90, s3, -v3 op_sel:[0,0,1] op_sel_hi:[0,0,1]
	v_cvt_pk_f16_f32 v4, v4, v5
	v_cvt_pk_f16_f32 v5, v6, v7
	v_cvt_pk_f16_f32 v6, v24, v25
	v_cvt_pk_f16_f32 v7, v26, v27
	s_nop 0
	v_mfma_f32_32x32x16_f16 a[0:15], v[4:7], v[8:11], a[0:15]
	v_mul_f32_e32 v8, 0x43800000, v99
	v_mul_f32_e32 v9, 0x43800000, v85
	v_mul_f32_e32 v10, 0x43800000, v86
	v_mul_f32_e32 v11, 0x43800000, v87
	v_mfma_f32_32x32x16_f16 a[16:31], v[4:7], v[16:19], a[16:31]
	v_mul_f32_e32 v4, 0x43800000, v100
	v_mul_f32_e32 v5, 0x43800000, v96
	v_mul_f32_e32 v6, 0x43800000, v97
	v_mul_f32_e32 v7, 0x43800000, v98
	v_cvt_pk_f16_f32 v4, v4, v5
	v_cvt_pk_f16_f32 v5, v6, v7
	v_cvt_pk_f16_f32 v6, v8, v9
	v_mfma_f32_32x32x16_f16 a[0:15], v[0:3], v[12:15], a[0:15]
	ds_read_b128 v[12:15], v74 offset:8896
	ds_read_b128 v[16:19], v74 offset:8928
	v_cvt_pk_f16_f32 v7, v10, v11
	ds_read_b128 v[8:11], v74 offset:224
	v_fma_mix_f32 v24, v99, s3, -v6 op_sel_hi:[0,0,1]
	v_fma_mix_f32 v25, v85, s3, -v6 op_sel:[0,0,1] op_sel_hi:[0,0,1]
	v_fma_mix_f32 v26, v86, s3, -v7 op_sel_hi:[0,0,1]
	v_mfma_f32_32x32x16_f16 a[16:31], v[0:3], v[20:23], a[16:31]
	ds_read_b128 v[0:3], v74 offset:192
	v_fma_mix_f32 v20, v100, s3, -v4 op_sel_hi:[0,0,1]
	v_fma_mix_f32 v21, v96, s3, -v4 op_sel:[0,0,1] op_sel_hi:[0,0,1]
	v_fma_mix_f32 v22, v97, s3, -v5 op_sel_hi:[0,0,1]
	v_fma_mix_f32 v23, v98, s3, -v5 op_sel:[0,0,1] op_sel_hi:[0,0,1]
	v_fma_mix_f32 v27, v87, s3, -v7 op_sel:[0,0,1] op_sel_hi:[0,0,1]
	v_cvt_pk_f16_f32 v20, v20, v21
	s_waitcnt lgkmcnt(0)
	v_mfma_f32_32x32x16_f16 a[0:15], v[4:7], v[0:3], a[0:15]
	v_cvt_pk_f16_f32 v21, v22, v23
	v_cvt_pk_f16_f32 v22, v24, v25
	v_cvt_pk_f16_f32 v23, v26, v27
	v_mul_f32_e32 v24, 0x43800000, v80
	v_mul_f32_e32 v25, 0x43800000, v81
	v_mul_f32_e32 v26, 0x43800000, v82
	v_mul_f32_e32 v27, 0x43800000, v83
	v_mfma_f32_32x32x16_f16 a[16:31], v[4:7], v[12:15], a[16:31]
	v_or_b32_e32 v74, s2, v76
	v_mfma_f32_32x32x16_f16 a[0:15], v[20:23], v[0:3], a[0:15]
	v_mfma_f32_32x32x16_f16 a[16:31], v[20:23], v[12:15], a[16:31]
	ds_read_b128 v[0:3], v40 offset:192
	ds_read_b128 v[12:15], v40 offset:224
	ds_read_b128 v[20:23], v40 offset:8928
	s_waitcnt lgkmcnt(2)
	v_mfma_f32_32x32x16_f16 a[0:15], v[4:7], v[0:3], a[0:15]
	ds_read_b128 v[0:3], v40 offset:8896
	s_waitcnt lgkmcnt(0)
	v_mfma_f32_32x32x16_f16 a[16:31], v[4:7], v[0:3], a[16:31]
	v_mul_f32_e32 v2, 0x43800000, v77
	v_mul_f32_e32 v3, 0x43800000, v78
	v_mul_f32_e32 v4, 0x43800000, v79
	v_cvt_pk_f16_f32 v0, v24, v25
	v_cvt_pk_f16_f32 v1, v26, v27
	v_cvt_pk_f16_f32 v2, v28, v2
	v_cvt_pk_f16_f32 v3, v3, v4
	s_nop 0
	v_mfma_f32_32x32x16_f16 a[0:15], v[0:3], v[8:11], a[0:15]
	v_fma_mix_f32 v4, v80, s3, -v0 op_sel_hi:[0,0,1]
	v_fma_mix_f32 v5, v81, s3, -v0 op_sel:[0,0,1] op_sel_hi:[0,0,1]
	v_fma_mix_f32 v6, v82, s3, -v1 op_sel_hi:[0,0,1]
	v_fma_mix_f32 v7, v83, s3, -v1 op_sel:[0,0,1] op_sel_hi:[0,0,1]
	v_fma_mix_f32 v24, v84, s3, -v2 op_sel_hi:[0,0,1]
	v_fma_mix_f32 v25, v77, s3, -v2 op_sel:[0,0,1] op_sel_hi:[0,0,1]
	v_fma_mix_f32 v26, v78, s3, -v3 op_sel_hi:[0,0,1]
	v_mfma_f32_32x32x16_f16 a[16:31], v[0:3], v[16:19], a[16:31]
	v_fma_mix_f32 v27, v79, s3, -v3 op_sel:[0,0,1] op_sel_hi:[0,0,1]
	v_cvt_pk_f16_f32 v4, v4, v5
	v_cvt_pk_f16_f32 v5, v6, v7
	v_cvt_pk_f16_f32 v6, v24, v25
	v_cvt_pk_f16_f32 v7, v26, v27
	s_nop 0
	v_mfma_f32_32x32x16_f16 a[0:15], v[4:7], v[8:11], a[0:15]
	v_mfma_f32_32x32x16_f16 a[16:31], v[4:7], v[16:19], a[16:31]
	v_mfma_f32_32x32x16_f16 a[0:15], v[0:3], v[12:15], a[0:15]
	v_mfma_f32_32x32x16_f16 a[16:31], v[0:3], v[20:23], a[16:31]
	v_lshlrev_b64 v[0:1], 8, v[74:75]
	v_lshl_add_u64 v[0:1], s[12:13], 0, v[0:1]
	v_lshl_add_u64 v[2:3], v[0:1], 0, s[0:1]
	v_lshl_add_u64 v[0:1], v[0:1], 0, v[72:73]
	s_nop 6
	v_accvgpr_read_b32 v4, a0
	v_accvgpr_read_b32 v5, a1
	v_mul_f32_e32 v4, 0x39b8aa3b, v4
	v_mul_f32_e32 v5, 0x39b8aa3b, v5
	v_cvt_pk_f16_f32 v4, v4, v5
	v_accvgpr_read_b32 v5, a2
	v_mul_f32_e32 v5, 0x39b8aa3b, v5
	v_accvgpr_read_b32 v6, a3
	v_mul_f32_e32 v6, 0x39b8aa3b, v6
	v_cvt_pk_f16_f32 v5, v5, v6
	global_store_dwordx2 v[0:1], v[4:5], off
	v_accvgpr_read_b32 v4, a16
	v_accvgpr_read_b32 v5, a17
	v_mul_f32_e32 v4, 0x39b8aa3b, v4
	v_mul_f32_e32 v5, 0x39b8aa3b, v5
	v_cvt_pk_f16_f32 v4, v4, v5
	v_accvgpr_read_b32 v5, a18
	v_accvgpr_read_b32 v6, a19
	v_mul_f32_e32 v5, 0x39b8aa3b, v5
	v_mul_f32_e32 v6, 0x39b8aa3b, v6
	v_cvt_pk_f16_f32 v5, v5, v6
	v_lshl_add_u64 v[6:7], v[2:3], 0, v[72:73]
	global_store_dwordx2 v[6:7], v[4:5], off
	v_accvgpr_read_b32 v4, a4
	v_accvgpr_read_b32 v5, a5
	v_mul_f32_e32 v4, 0x39b8aa3b, v4
	v_mul_f32_e32 v5, 0x39b8aa3b, v5
	v_cvt_pk_f16_f32 v4, v4, v5
	v_accvgpr_read_b32 v5, a6
	v_mul_f32_e32 v5, 0x39b8aa3b, v5
	v_accvgpr_read_b32 v6, a7
	v_mul_f32_e32 v6, 0x39b8aa3b, v6
	v_cvt_pk_f16_f32 v5, v5, v6
	global_store_dwordx2 v[0:1], v[4:5], off offset:16
	v_accvgpr_read_b32 v4, a20
	v_accvgpr_read_b32 v5, a21
	v_mul_f32_e32 v4, 0x39b8aa3b, v4
	v_mul_f32_e32 v5, 0x39b8aa3b, v5
	v_cvt_pk_f16_f32 v4, v4, v5
	v_accvgpr_read_b32 v5, a22
	v_accvgpr_read_b32 v6, a23
	v_mul_f32_e32 v5, 0x39b8aa3b, v5
	v_mul_f32_e32 v6, 0x39b8aa3b, v6
	v_cvt_pk_f16_f32 v5, v5, v6
	v_or_b32_e32 v6, 16, v72
	v_mov_b32_e32 v7, v73
	v_lshl_add_u64 v[6:7], v[2:3], 0, v[6:7]
	global_store_dwordx2 v[6:7], v[4:5], off
	v_accvgpr_read_b32 v4, a8
	v_accvgpr_read_b32 v5, a9
	v_mul_f32_e32 v4, 0x39b8aa3b, v4
	v_mul_f32_e32 v5, 0x39b8aa3b, v5
	v_cvt_pk_f16_f32 v4, v4, v5
	v_accvgpr_read_b32 v5, a10
	v_mul_f32_e32 v5, 0x39b8aa3b, v5
	v_accvgpr_read_b32 v6, a11
	v_mul_f32_e32 v6, 0x39b8aa3b, v6
	v_cvt_pk_f16_f32 v5, v5, v6
	global_store_dwordx2 v[0:1], v[4:5], off offset:32
	v_accvgpr_read_b32 v4, a24
	v_accvgpr_read_b32 v5, a25
	v_mul_f32_e32 v4, 0x39b8aa3b, v4
	v_mul_f32_e32 v5, 0x39b8aa3b, v5
	v_cvt_pk_f16_f32 v4, v4, v5
	v_accvgpr_read_b32 v5, a26
	v_accvgpr_read_b32 v6, a27
	v_mul_f32_e32 v5, 0x39b8aa3b, v5
	v_mul_f32_e32 v6, 0x39b8aa3b, v6
	v_cvt_pk_f16_f32 v5, v5, v6
	v_or_b32_e32 v6, 32, v72
	v_mov_b32_e32 v7, v73
	v_lshl_add_u64 v[6:7], v[2:3], 0, v[6:7]
	global_store_dwordx2 v[6:7], v[4:5], off
	v_accvgpr_read_b32 v4, a12
	v_accvgpr_read_b32 v5, a13
	v_mul_f32_e32 v4, 0x39b8aa3b, v4
	v_mul_f32_e32 v5, 0x39b8aa3b, v5
	v_cvt_pk_f16_f32 v4, v4, v5
	v_accvgpr_read_b32 v5, a14
	v_mul_f32_e32 v5, 0x39b8aa3b, v5
	v_accvgpr_read_b32 v6, a15
	v_mul_f32_e32 v6, 0x39b8aa3b, v6
	v_cvt_pk_f16_f32 v5, v5, v6
	global_store_dwordx2 v[0:1], v[4:5], off offset:48
	v_accvgpr_read_b32 v0, a28
	v_accvgpr_read_b32 v1, a29
	v_mul_f32_e32 v0, 0x39b8aa3b, v0
	v_mul_f32_e32 v1, 0x39b8aa3b, v1
	v_cvt_pk_f16_f32 v0, v0, v1
	v_accvgpr_read_b32 v1, a30
	v_or_b32_e32 v72, 48, v72
	v_mul_f32_e32 v1, 0x39b8aa3b, v1
	v_accvgpr_read_b32 v4, a31
	v_lshl_add_u64 v[2:3], v[2:3], 0, v[72:73]
	v_mul_f32_e32 v4, 0x39b8aa3b, v4
	v_cvt_pk_f16_f32 v1, v1, v4
	global_store_dwordx2 v[2:3], v[0:1], off
	s_endpgm

	.amdhsa_kernel _Z11prep_kernelPKfS0_S0_S0_PDF16_S1_S0_S1_
		.amdhsa_group_segment_fixed_size 34816
		.amdhsa_private_segment_fixed_size 0
		.amdhsa_kernarg_size 64
		.amdhsa_user_sgpr_count 2
		.amdhsa_user_sgpr_dispatch_ptr 0
		.amdhsa_user_sgpr_queue_ptr 0
		.amdhsa_user_sgpr_kernarg_segment_ptr 1
		.amdhsa_user_sgpr_dispatch_id 0
		.amdhsa_user_sgpr_kernarg_preload_length 0
		.amdhsa_user_sgpr_kernarg_preload_offset 0
		.amdhsa_user_sgpr_private_segment_size 0
		.amdhsa_uses_dynamic_stack 0
		.amdhsa_enable_private_segment 0
		.amdhsa_system_sgpr_workgroup_id_x 1
		.amdhsa_system_sgpr_workgroup_id_y 0
		.amdhsa_system_sgpr_workgroup_id_z 0
		.amdhsa_system_sgpr_workgroup_info 0
		.amdhsa_system_vgpr_workitem_id 0
		.amdhsa_next_free_vgpr 220
		.amdhsa_next_free_sgpr 96
		.amdhsa_accum_offset 188
		.amdhsa_reserve_vcc 1
		.amdhsa_float_round_mode_32 0
		.amdhsa_float_round_mode_16_64 0
		.amdhsa_float_denorm_mode_32 3
		.amdhsa_float_denorm_mode_16_64 3
		.amdhsa_dx10_clamp 1
		.amdhsa_ieee_mode 1
		.amdhsa_fp16_overflow 0
		.amdhsa_tg_split 0
		.amdhsa_exception_fp_ieee_invalid_op 0
		.amdhsa_exception_fp_denorm_src 0
		.amdhsa_exception_fp_ieee_div_zero 0
		.amdhsa_exception_fp_ieee_overflow 0
		.amdhsa_exception_fp_ieee_underflow 0
		.amdhsa_exception_fp_ieee_inexact 0
		.amdhsa_exception_int_div_zero 0
	.end_amdhsa_kernel

_Z11attn_kernelPKDF16_S0_PDF16_P15HIP_vector_typeIfLj2EE:
	s_getpc_b64 s[38:39]
	v_lshlrev_b32_e32 v240, 7, v0
	v_min_u32_e32 v240, 0x3380, v240
	global_load_dword v241, v240, s[38:39]
	s_mov_b32 s5, 0
	s_mov_b32 s28, s3
	s_load_dwordx8 s[20:27], s[0:1], 0x0
	s_mov_b32 s3, s5
	s_lshl_b64 s[0:1], s[4:5], 12
	s_lshl_b64 s[2:3], s[2:3], 8
	s_add_u32 s0, s0, s2
	v_lshrrev_b32_e32 v1, 6, v0
	s_addc_u32 s1, s1, s3
	v_and_b32_e32 v160, 31, v0
	s_lshl_b64 s[2:3], s[0:1], 8
	v_lshlrev_b32_e32 v162, 5, v1
	s_waitcnt lgkmcnt(0)
	s_add_u32 s2, s20, s2
	v_or_b32_e32 v2, v162, v160
	v_bfe_u32 v54, v0, 5, 1
	s_addc_u32 s3, s21, s3
	v_lshlrev_b32_e32 v164, 8, v2
	v_mov_b32_e32 v165, 0
	v_lshl_add_u64 v[2:3], s[2:3], 0, v[164:165]
	v_lshlrev_b32_e32 v164, 4, v54
	v_lshl_add_u64 v[2:3], v[2:3], 0, v[164:165]
	global_load_dwordx4 v[156:159], v[2:3], off
	global_load_dwordx4 v[152:155], v[2:3], off offset:32
	global_load_dwordx4 v[148:151], v[2:3], off offset:64
	global_load_dwordx4 v[144:147], v[2:3], off offset:96
	global_load_dwordx4 v[140:143], v[2:3], off offset:128
	global_load_dwordx4 v[136:139], v[2:3], off offset:160
	global_load_dwordx4 v[132:135], v[2:3], off offset:192
	global_load_dwordx4 v[128:131], v[2:3], off offset:224
	s_ashr_i32 s29, s28, 31
	v_bfe_u32 v55, v0, 2, 3
	s_lshl_b64 s[2:3], s[4:5], 20
	s_lshl_b64 s[20:21], s[28:29], 18
	v_lshl_or_b32 v2, v1, 3, v55
	s_add_u32 s4, s22, s2
	v_lshrrev_b32_e32 v3, 2, v2
	s_addc_u32 s7, s23, s3
	v_xor_b32_e32 v4, v3, v0
	s_add_u32 s6, s4, s20
	v_and_b32_e32 v5, 32, v0
	v_lshlrev_b32_e32 v4, 3, v4
	v_lshlrev_b32_e32 v1, 11, v1
	s_addc_u32 s7, s7, s21
	v_lshlrev_b32_e32 v164, 8, v2
	v_and_or_b32 v4, v4, 24, v5
	v_add_u32_e32 v173, 0, v1
	v_lshl_add_u64 v[2:3], s[6:7], 0, v[164:165]
	v_lshlrev_b32_e32 v164, 1, v4
	v_readfirstlane_b32 s4, v173
	v_add_u32_e32 v6, 0x400, v173
	v_lshl_add_u64 v[2:3], v[2:3], 0, v[164:165]
	s_mov_b64 s[6:7], 0x80
	s_mov_b32 m0, s4
	v_readfirstlane_b32 s4, v6
	v_add_u32_e32 v6, 0x4000, v173
	v_lshl_add_u64 v[4:5], v[2:3], 0, s[6:7]
	global_load_lds_dwordx4 v[2:3], off
	s_mov_b32 m0, s4
	s_mov_b64 s[6:7], 0x4000
	v_readfirstlane_b32 s4, v6
	global_load_lds_dwordx4 v[4:5], off
	v_lshl_add_u64 v[4:5], v[2:3], 0, s[6:7]
	s_mov_b32 m0, s4
	s_mov_b64 s[6:7], 0x4080
	global_load_lds_dwordx4 v[4:5], off
	v_add_u32_e32 v4, 0x4400, v173
	v_lshl_add_u64 v[2:3], v[2:3], 0, s[6:7]
	v_readfirstlane_b32 s4, v4
	s_mov_b32 m0, s4
	s_movk_i32 s4, 0x1c0
	global_load_lds_dwordx4 v[2:3], off
	v_lshlrev_b32_e32 v2, 8, v0
	v_and_b32_e32 v2, 0x1800, v2
	v_lshlrev_b32_e32 v3, 6, v0
	v_and_or_b32 v6, v3, s4, v2
	v_xor_b32_e32 v2, v54, v55
	v_lshlrev_b32_e32 v2, 4, v2
	v_and_or_b32 v175, v2, 48, v6
	s_waitcnt vmcnt(2)
	v_add_u32_e32 v172, 0, v175
	s_waitcnt lgkmcnt(0)
	s_barrier
	ds_read_b128 v[2:5], v172
	ds_read_b128 v[34:37], v172 offset:512
	v_bitop3_b32 v7, v54, v55, 2 bitop3:0x36
	v_lshlrev_b32_e32 v7, 4, v7
	v_and_or_b32 v176, v7, 48, v6
	v_add_u32_e32 v174, 0, v176
	ds_read_b128 v[18:21], v174
	ds_read_b128 v[38:41], v174 offset:512
	s_mov_b32 s33, 0x41200000
	s_cmp_lg_u32 0, -1
	s_cselect_b32 s37, 0, 0
	s_waitcnt vmcnt(0) lgkmcnt(0)
	v_mfma_f32_32x32x16_f16 v[2:17], v[2:5], v[156:159], 0
	s_movk_i32 s4, 0x110
	v_and_b32_e32 v161, 63, v0
	v_lshl_or_b32 v1, v55, 8, v1
	s_mov_b32 s18, s5
	s_mov_b32 s19, s5
	s_mov_b32 s6, s5
	s_mov_b32 s7, s5
	v_mfma_f32_32x32x16_f16 v[2:17], v[18:21], v[152:155], v[2:17]
	ds_read_b128 v[18:21], v172 offset:8192
	ds_read_b128 v[42:45], v172 offset:8704
	ds_read_b128 v[46:49], v174 offset:8192
	ds_read_b128 v[50:53], v174 offset:8704
	s_mov_b32 s8, s5
	s_mov_b32 s9, s5
	s_mov_b32 s10, s5
	s_mov_b32 s11, s5
	s_mov_b32 s12, s5
	s_waitcnt lgkmcnt(3)
	v_mfma_f32_32x32x16_f16 v[18:33], v[18:21], v[156:159], 0
	s_mov_b32 s13, s5
	s_mov_b32 s14, s5
	s_mov_b32 s15, s5
	s_mov_b32 s16, s5
	s_mov_b32 s17, s5
	s_mov_b32 s36, 1
	s_mov_b32 s34, -1
	s_waitcnt lgkmcnt(1)
	v_mfma_f32_32x32x16_f16 v[18:33], v[46:49], v[152:155], v[18:33]
	s_mov_b32 s35, 2
	s_mov_b64 s[30:31], 0x8000
	v_mfma_f32_32x32x16_f16 v[2:17], v[34:37], v[148:151], v[2:17]
	v_mfma_f32_32x32x16_f16 v[18:33], v[42:45], v[148:151], v[18:33]
	v_mfma_f32_32x32x16_f16 v[2:17], v[38:41], v[144:147], v[2:17]
	ds_read_b128 v[34:37], v172 offset:1024
	ds_read_b128 v[38:41], v172 offset:1536
	s_waitcnt lgkmcnt(2)
	v_mfma_f32_32x32x16_f16 v[18:33], v[50:53], v[144:147], v[18:33]
	s_waitcnt lgkmcnt(1)
	v_mfma_f32_32x32x16_f16 v[2:17], v[34:37], v[140:143], v[2:17]
	ds_read_b128 v[34:37], v172 offset:9216
	ds_read_b128 v[42:45], v172 offset:9728
	s_waitcnt lgkmcnt(1)
	v_mfma_f32_32x32x16_f16 v[18:33], v[34:37], v[140:143], v[18:33]
	ds_read_b128 v[34:37], v174 offset:1024
	ds_read_b128 v[46:49], v174 offset:1536
	s_waitcnt lgkmcnt(1)
	v_mfma_f32_32x32x16_f16 v[2:17], v[34:37], v[136:139], v[2:17]
	ds_read_b128 v[34:37], v174 offset:9216
	ds_read_b128 v[50:53], v174 offset:9728
	v_mfma_f32_32x32x16_f16 v[2:17], v[38:41], v[132:135], v[2:17]
	s_waitcnt lgkmcnt(1)
	v_mfma_f32_32x32x16_f16 v[18:33], v[34:37], v[136:139], v[18:33]
	v_mov_b32_e32 v34, 0xf149f2ca
	v_mfma_f32_32x32x16_f16 v[2:17], v[46:49], v[128:131], v[2:17]
	v_mfma_f32_32x32x16_f16 v[18:33], v[42:45], v[132:135], v[18:33]
	s_nop 10
	v_max_f32_e32 v35, v3, v3
	v_max_f32_e32 v36, v2, v2
	v_max_f32_e32 v35, v36, v35
	v_max3_f32 v35, v35, v4, v5
	v_max3_f32 v35, v35, v6, v7
	v_max3_f32 v35, v35, v8, v9
	v_max3_f32 v35, v35, v10, v11
	s_waitcnt lgkmcnt(0)
	v_mfma_f32_32x32x16_f16 v[18:33], v[50:53], v[128:131], v[18:33]
	v_max3_f32 v35, v35, v12, v13
	v_max3_f32 v35, v35, v14, v15
	v_max3_f32 v35, v35, v16, v17
	s_nop 8
	v_max3_f32 v35, v35, v18, v19
	v_max3_f32 v35, v35, v20, v21
	v_max3_f32 v35, v35, v22, v23
	v_max3_f32 v35, v35, v24, v25
	v_max3_f32 v35, v35, v26, v27
	v_max3_f32 v35, v35, v28, v29
	v_max3_f32 v35, v35, v30, v31
	v_max3_f32 v35, v35, v32, v33
	v_mov_b32_e32 v36, v35
	s_nop 1
	v_permlane32_swap_b32_e32 v35, v36
	v_max_f32_e32 v36, v36, v36
	v_max_f32_e32 v35, v35, v35
	v_max_f32_e32 v35, v35, v36
	v_add_f32_e32 v36, 0x7149f2ca, v35
	v_cmp_ge_f32_e32 vcc, s33, v36
	s_cmp_eq_u64 vcc, exec
	v_max_f32_e32 v35, 0xf149f2ca, v35
	s_cselect_b64 vcc, -1, 0
	v_cndmask_b32_e32 v168, v35, v34, vcc
	v_sub_f32_e32 v96, v18, v168
	v_sub_f32_e32 v97, v19, v168
	v_lshlrev_b32_e32 v18, 4, v0
	v_lshrrev_b32_e32 v19, 4, v0
	v_sub_f32_e32 v98, v20, v168
	v_and_b32_e32 v18, 0xc0, v18
	v_bitop3_b32 v19, v19, v54, 1 bitop3:0x6c
	v_lshlrev_b32_e32 v20, 3, v0
	v_sub_f32_e32 v99, v21, v168
	v_lshl_or_b32 v18, v54, 11, v18
	v_lshlrev_b32_e32 v19, 5, v19
	v_and_b32_e32 v21, 8, v20
	v_or3_b32 v18, v18, v21, v19
	v_and_b32_e32 v19, 16, v20
	v_sub_f32_e32 v0, 0xf149f2ca, v35
	v_add3_u32 v163, v19, s37, v18
	v_bitop3_b32 v169, v18, s4, v19 bitop3:0x36
	v_exp_f32_e32 v18, v0
	s_add_u32 s2, s2, s20
	v_sub_f32_e32 v2, v2, v168
	v_sub_f32_e32 v3, v3, v168
	v_sub_f32_e32 v4, v4, v168
	v_sub_f32_e32 v5, v5, v168
	v_sub_f32_e32 v6, v6, v168
	v_sub_f32_e32 v7, v7, v168
	v_sub_f32_e32 v8, v8, v168
	v_sub_f32_e32 v9, v9, v168
	v_sub_f32_e32 v10, v10, v168
	v_sub_f32_e32 v11, v11, v168
	v_sub_f32_e32 v12, v12, v168
	v_sub_f32_e32 v13, v13, v168
	v_sub_f32_e32 v14, v14, v168
	v_sub_f32_e32 v15, v15, v168
	v_sub_f32_e32 v16, v16, v168
	v_sub_f32_e32 v17, v17, v168
	s_addc_u32 s3, s3, s21
	s_mov_b32 s4, s5
	v_exp_f32_e32 v127, v2
	v_exp_f32_e32 v180, v3
	v_exp_f32_e32 v125, v4
	v_exp_f32_e32 v179, v5
	v_exp_f32_e32 v123, v6
	v_exp_f32_e32 v126, v7
	v_exp_f32_e32 v122, v8
	v_exp_f32_e32 v124, v9
	v_exp_f32_e32 v119, v10
	v_exp_f32_e32 v121, v11
	v_exp_f32_e32 v117, v12
	v_exp_f32_e32 v120, v13
	v_exp_f32_e32 v115, v14
	v_exp_f32_e32 v118, v15
	v_exp_f32_e32 v114, v16
	v_exp_f32_e32 v116, v17
	v_or3_b32 v0, s2, v1, v164
	v_mov_b32_e32 v1, s3
	v_lshlrev_b32_e32 v164, 3, v54
	v_mov_b64_e32 v[62:63], s[18:19]
	v_lshl_add_u64 v[0:1], s[22:23], 0, v[0:1]
	s_mov_b64 s[2:3], 0xc080
	v_mov_b64_e32 v[48:49], s[4:5]
	v_sub_f32_e32 v100, v22, v168
	v_sub_f32_e32 v101, v23, v168
	v_sub_f32_e32 v102, v24, v168
	v_sub_f32_e32 v103, v25, v168
	v_sub_f32_e32 v104, v26, v168
	v_sub_f32_e32 v105, v27, v168
	v_sub_f32_e32 v106, v28, v168
	v_sub_f32_e32 v107, v29, v168
	v_sub_f32_e32 v108, v30, v168
	v_sub_f32_e32 v109, v31, v168
	v_sub_f32_e32 v110, v32, v168
	v_sub_f32_e32 v111, v33, v168
	v_lshl_add_u64 v[170:171], v[0:1], 0, s[2:3]
	s_movk_i32 s2, 0xbf80
	s_movk_i32 s20, 0xc000
	s_movk_i32 s22, 0xff80
	v_mov_b32_e32 v166, 1.0
	v_mov_b64_e32 v[60:61], s[16:17]
	v_mov_b64_e32 v[58:59], s[14:15]
	v_mov_b64_e32 v[56:57], s[12:13]
	v_mov_b64_e32 v[54:55], s[10:11]
	v_mov_b64_e32 v[52:53], s[8:9]
	v_mov_b64_e32 v[50:51], s[6:7]
	v_mov_b64_e32 v[32:33], v[48:49]
	v_mov_b64_e32 v[16:17], v[48:49]
	v_mov_b64_e32 v[0:1], v[48:49]
	s_mov_b32 s3, -1
	s_mov_b32 s21, -1
	s_mov_b32 s23, -1
	v_add_u32_e32 v167, s37, v169
	v_mov_b64_e32 v[34:35], v[50:51]
	v_mov_b64_e32 v[36:37], v[52:53]
	v_mov_b64_e32 v[38:39], v[54:55]
	v_mov_b64_e32 v[40:41], v[56:57]
	v_mov_b64_e32 v[42:43], v[58:59]
	v_mov_b64_e32 v[44:45], v[60:61]
	v_mov_b64_e32 v[46:47], v[62:63]
	v_mov_b64_e32 v[18:19], v[50:51]
	v_mov_b64_e32 v[20:21], v[52:53]
	v_mov_b64_e32 v[22:23], v[54:55]
	v_mov_b64_e32 v[24:25], v[56:57]
	v_mov_b64_e32 v[26:27], v[58:59]
	v_mov_b64_e32 v[28:29], v[60:61]
	v_mov_b64_e32 v[30:31], v[62:63]
	v_mov_b64_e32 v[2:3], v[50:51]
	v_mov_b64_e32 v[4:5], v[52:53]
	v_mov_b64_e32 v[6:7], v[54:55]
	v_mov_b64_e32 v[8:9], v[56:57]
	v_mov_b64_e32 v[10:11], v[58:59]
	v_mov_b64_e32 v[12:13], v[60:61]
	v_mov_b64_e32 v[14:15], v[62:63]

amdhsa.kernels:
  - .agpr_count:     32
    .args:
      - .actual_access:  read_only
        .address_space:  global
        .offset:         0
        .size:           8
        .value_kind:     global_buffer
      - .actual_access:  read_only
        .address_space:  global
        .offset:         8
        .size:           8
        .value_kind:     global_buffer
      - .actual_access:  read_only
        .address_space:  global
        .offset:         16
        .size:           8
        .value_kind:     global_buffer
      - .actual_access:  read_only
        .address_space:  global
        .offset:         24
        .size:           8
        .value_kind:     global_buffer
      - .actual_access:  write_only
        .address_space:  global
        .offset:         32
        .size:           8
        .value_kind:     global_buffer
      - .actual_access:  write_only
        .address_space:  global
        .offset:         40
        .size:           8
        .value_kind:     global_buffer
      - .actual_access:  read_only
        .address_space:  global
        .offset:         48
        .size:           8
        .value_kind:     global_buffer
      - .actual_access:  write_only
        .address_space:  global
        .offset:         56
        .size:           8
        .value_kind:     global_buffer
    .group_segment_fixed_size: 34816
    .kernarg_segment_align: 8
    .kernarg_segment_size: 64
    .language:       OpenCL C
    .language_version:
      - 2
      - 0
    .max_flat_workgroup_size: 256
    .name:           _Z11prep_kernelPKfS0_S0_S0_PDF16_S1_S0_S1_
    .private_segment_fixed_size: 0
    .sgpr_count:     30
    .sgpr_spill_count: 0
    .symbol:         _Z11prep_kernelPKfS0_S0_S0_PDF16_S1_S0_S1_.kd
    .uniform_work_group_size: 1
    .uses_dynamic_stack: false
    .vgpr_count:     220
    .vgpr_spill_count: 0
    .wavefront_size: 64
  - .agpr_count:     0
    .args:
      - .actual_access:  read_only
        .address_space:  global
        .offset:         0
        .size:           8
        .value_kind:     global_buffer
      - .address_space:  global
        .offset:         8
        .size:           8
        .value_kind:     global_buffer
      - .actual_access:  write_only
        .address_space:  global
        .offset:         16
        .size:           8
        .value_kind:     global_buffer
      - .actual_access:  write_only
        .address_space:  global
        .offset:         24
        .size:           8
        .value_kind:     global_buffer
    .group_segment_fixed_size: 0
    .kernarg_segment_align: 8
    .kernarg_segment_size: 32
    .language:       OpenCL C
    .language_version:
      - 2
      - 0
    .max_flat_workgroup_size: 512
    .name:           _Z11attn_kernelPKDF16_S0_PDF16_P15HIP_vector_typeIfLj2EE
    .private_segment_fixed_size: 0
    .sgpr_count:     46
    .sgpr_spill_count: 0
    .symbol:         _Z11attn_kernelPKDF16_S0_PDF16_P15HIP_vector_typeIfLj2EE.kd
    .uniform_work_group_size: 1
    .uses_dynamic_stack: false
    .vgpr_count:     244
    .vgpr_spill_count: 0
    .wavefront_size: 64
  - .agpr_count:     0
    .args:
      - .actual_access:  read_only
        .address_space:  global
        .offset:         0
        .size:           8
        .value_kind:     global_buffer
      - .actual_access:  read_only
        .address_space:  global
        .offset:         8
        .size:           8
        .value_kind:     global_buffer
      - .actual_access:  read_only
        .address_space:  global
        .offset:         16
        .size:           8
        .value_kind:     global_buffer
      - .actual_access:  read_only
        .address_space:  global
        .offset:         24
        .size:           8
        .value_kind:     global_buffer
      - .actual_access:  write_only
        .address_space:  global
        .offset:         32
        .size:           8
        .value_kind:     global_buffer
    .group_segment_fixed_size: 17408
    .kernarg_segment_align: 8
    .kernarg_segment_size: 40
    .language:       OpenCL C
    .language_version:
      - 2
      - 0
    .max_flat_workgroup_size: 256
    .name:           _Z19combine_proj_kernelPKDF16_PK15HIP_vector_typeIfLj2EES0_PKfPf
    .private_segment_fixed_size: 0
    .sgpr_count:     42
    .sgpr_spill_count: 0
    .symbol:         _Z19combine_proj_kernelPKDF16_PK15HIP_vector_typeIfLj2EES0_PKfPf.kd
    .uniform_work_group_size: 1
    .uses_dynamic_stack: false
    .vgpr_count:     220
    .vgpr_spill_count: 0
    .wavefront_size: 64
